# baseline (speedup 1.0000x reference)
_Z9proj_gemmPKfS0_S0_PK14__hip_bfloat16S0_S0_S0_PS1_:
	s_lshl_b32 s3, s2, 2
	s_load_dwordx8 s[8:15], s[0:1], 0x0
	s_and_b32 s3, s3, 28
	s_bfe_u32 s30, s2, 0x20005
	s_lshr_b32 s6, s2, 3
	s_ashr_i32 s18, s2, 7
	s_lshr_b32 s7, s2, 5
	s_or_b32 s20, s3, s30
	s_bfe_u32 s3, s2, 0x20003
	s_cmpk_lt_u32 s2, 0x80
	s_cselect_b64 s[16:17], -1, 0
	s_and_b64 s[4:5], s[16:17], exec
	s_waitcnt lgkmcnt(0)
	s_cselect_b32 s4, s9, s11
	s_cselect_b32 s5, s8, s10
	s_lshl_b32 s24, s20, 18
	s_lshl_b32 s8, s20, 20
	s_add_u32 s25, s5, s8
	s_addc_u32 s26, s4, 0
	s_ashr_i32 s19, s18, 31
	s_lshl_b64 s[4:5], s[18:19], 21
	s_add_u32 s4, s14, s4
	s_addc_u32 s5, s15, s5
	s_lshl_b32 s8, s3, 19
	s_add_u32 s27, s4, s8
	s_addc_u32 s28, s5, 0
	s_xor_b32 s6, s6, s18
	v_lshlrev_b32_e32 v1, 4, v0
	s_lshl_b32 s34, s6, 4
	v_lshlrev_b32_e32 v2, 3, v0
	v_and_b32_e32 v3, 0x1f0, v1
	s_movk_i32 s6, 0x200
	s_lshl_b32 s4, s20, 1
	s_mul_i32 s31, s18, 5
	s_xor_b32 s7, s7, s18
	v_lshrrev_b32_e32 v28, 6, v0
	s_and_b32 s35, s34, 16
	v_and_or_b32 v29, v2, s6, v3
	v_lshrrev_b32_e32 v2, 1, v0
	v_and_b32_e32 v3, 48, v1
	s_add_i32 s4, s4, s31
	v_bitop3_b32 v2, v2, v3, 32 bitop3:0x6c
	v_or_b32_e32 v30, s35, v28
	s_lshl_b32 s38, s7, 4
	s_and_b32 s5, s4, 15
	v_lshrrev_b32_e32 v2, 1, v2
	v_or_b32_e32 v32, 8, v30
	s_and_b32 s39, s38, 16
	v_and_or_b32 v178, v0, 32, v2
	v_lshlrev_b32_e32 v2, 3, v30
	v_lshrrev_b32_e32 v31, 6, v29
	s_movk_i32 s36, 0xb0
	v_lshlrev_b32_e32 v3, 3, v32
	s_movk_i32 s37, 0xf0
	v_or_b32_e32 v33, s39, v28
	s_lshl_b32 s33, s4, 6
	s_lshl_b32 s4, s5, 8
	v_and_or_b32 v2, v2, s36, v31
	v_and_or_b32 v12, v3, s37, v31
	v_lshlrev_b32_e32 v3, 3, v33
	v_or_b32_e32 v34, 8, v33
	s_add_u32 s20, s25, s4
	v_mov_b32_e32 v183, 0
	v_and_or_b32 v20, v3, s36, v31
	v_lshlrev_b32_e32 v3, 3, v34
	s_addc_u32 s21, s26, 0
	v_lshlrev_b32_e32 v180, 12, v2
	v_mov_b32_e32 v181, v183
	v_and_or_b32 v22, v3, s37, v31
	v_lshl_add_u64 v[2:3], s[20:21], 0, v[180:181]
	v_lshlrev_b32_e32 v182, 2, v178
	v_lshl_add_u64 v[10:11], v[2:3], 0, v[182:183]
	v_lshlrev_b32_e32 v184, 12, v12
	v_mov_b32_e32 v185, v183
	s_lshl_b32 s4, s5, 7
	global_load_dwordx4 v[2:5], v[10:11], off offset:16
	global_load_dwordx4 v[6:9], v[10:11], off
	v_lshl_add_u64 v[10:11], s[20:21], 0, v[184:185]
	s_add_u32 s22, s27, s4
	v_lshl_add_u64 v[14:15], v[10:11], 0, v[182:183]
	s_addc_u32 s23, s28, 0
	v_lshlrev_b32_e32 v186, 11, v20
	v_mov_b32_e32 v187, v183
	global_load_dwordx4 v[10:13], v[14:15], off offset:16
	global_load_dwordx4 v[16:19], v[14:15], off
	v_lshl_add_u64 v[20:21], s[22:23], 0, v[186:187]
	v_lshlrev_b32_e32 v14, 1, v178
	v_mov_b32_e32 v15, v183
	v_lshlrev_b32_e32 v188, 11, v22
	v_mov_b32_e32 v189, v183
	v_lshl_add_u64 v[24:25], v[20:21], 0, v[14:15]
	v_lshl_add_u64 v[20:21], s[22:23], 0, v[188:189]
	v_lshl_add_u64 v[26:27], v[20:21], 0, v[14:15]
	global_load_dwordx4 v[20:23], v[24:25], off
	global_load_dwordx4 v[50:53], v[26:27], off
	v_bfe_u32 v24, v0, 5, 1
	v_and_or_b32 v25, v30, 22, v24
	v_lshl_or_b32 v208, v25, 10, v29
	v_and_or_b32 v25, v32, 30, v24
	v_lshl_or_b32 v205, v25, 10, v29
	v_bitop3_b32 v25, s34, 16, v28 bitop3:0x26
	v_and_or_b32 v26, v25, 22, v24
	v_lshl_or_b32 v204, v26, 10, v29
	v_bitop3_b32 v26, s35, v28, 24 bitop3:0xde
	v_and_or_b32 v27, v26, 30, v24
	v_lshl_or_b32 v201, v27, 10, v29
	v_and_or_b32 v27, v33, 22, v24
	v_lshl_or_b32 v206, v27, 10, v29
	v_and_or_b32 v27, v34, 30, v24
	s_load_dwordx8 s[4:11], s[0:1], 0x20
	v_lshl_or_b32 v207, v27, 10, v29
	v_bitop3_b32 v27, s38, 16, v28 bitop3:0x26
	v_bitop3_b32 v28, s39, v28, 24 bitop3:0xde
	v_and_or_b32 v30, v27, 22, v24
	v_and_or_b32 v24, v28, 30, v24
	v_and_b32_e32 v179, 15, v0
	v_lshl_or_b32 v202, v30, 10, v29
	v_lshl_or_b32 v203, v24, 10, v29
	v_lshlrev_b32_e32 v24, 3, v28
	v_lshlrev_b32_e32 v29, 2, v0
	v_lshrrev_b32_e32 v198, 8, v0
	v_lshlrev_b32_e32 v25, 3, v25
	v_lshlrev_b32_e32 v26, 3, v26
	v_lshlrev_b32_e32 v27, 3, v27
	v_and_or_b32 v28, v24, s37, v31
	v_and_b32_e32 v24, 48, v0
	v_and_b32_e32 v29, 32, v29
	v_lshlrev_b32_e32 v30, 6, v179
	s_mov_b32 s29, 0
	v_and_b32_e32 v199, 63, v0
	v_and_or_b32 v25, v25, s36, v31
	v_and_or_b32 v26, v26, s37, v31
	v_bfe_u32 v200, v0, 6, 2
	v_and_or_b32 v27, v27, s36, v31
	v_lshlrev_b32_e32 v80, 14, v198
	v_bitop3_b32 v81, v30, v29, v24 bitop3:0x36
	v_lshlrev_b32_e32 v190, 12, v25
	v_mov_b32_e32 v191, v183
	v_lshl_add_u64 v[24:25], s[20:21], 0, v[190:191]
	v_lshl_add_u64 v[24:25], v[24:25], 0, v[182:183]
	v_lshlrev_b32_e32 v192, 12, v26
	v_mov_b32_e32 v193, v183
	global_load_dwordx4 v[54:57], v[24:25], off offset:16
	global_load_dwordx4 v[58:61], v[24:25], off
	v_lshl_add_u64 v[24:25], s[20:21], 0, v[192:193]
	v_lshl_add_u64 v[24:25], v[24:25], 0, v[182:183]
	v_lshlrev_b32_e32 v194, 11, v27
	v_mov_b32_e32 v195, v183
	global_load_dwordx4 v[62:65], v[24:25], off offset:16
	global_load_dwordx4 v[66:69], v[24:25], off
	v_lshl_add_u64 v[24:25], s[22:23], 0, v[194:195]
	v_lshlrev_b32_e32 v196, 11, v28
	v_mov_b32_e32 v197, v183
	v_lshl_add_u64 v[24:25], v[24:25], 0, v[14:15]
	v_lshl_add_u64 v[26:27], s[22:23], 0, v[196:197]
	v_lshl_add_u64 v[26:27], v[26:27], 0, v[14:15]
	global_load_dwordx4 v[70:73], v[24:25], off
	global_load_dwordx4 v[74:77], v[26:27], off
	s_add_i32 s33, s33, 64
	s_and_b32 s20, s33, 0x3c0
	s_lshl_b32 s0, s20, 2
	s_add_u32 s0, s25, s0
	s_addc_u32 s1, s26, 0
	v_lshl_add_u64 v[24:25], s[0:1], 0, v[180:181]
	v_lshl_add_u64 v[24:25], v[24:25], 0, v[182:183]
	s_lshl_b32 s20, s20, 1
	global_load_dwordx4 v[42:45], v[24:25], off offset:16
	global_load_dwordx4 v[46:49], v[24:25], off
	v_lshl_add_u64 v[24:25], s[0:1], 0, v[184:185]
	s_add_u32 s20, s27, s20
	v_lshl_add_u64 v[24:25], v[24:25], 0, v[182:183]
	s_addc_u32 s21, s28, 0
	global_load_dwordx4 v[34:37], v[24:25], off offset:16
	global_load_dwordx4 v[38:41], v[24:25], off
	v_lshl_add_u64 v[24:25], s[20:21], 0, v[186:187]
	v_lshl_add_u64 v[24:25], v[24:25], 0, v[14:15]
	v_lshl_add_u64 v[26:27], s[20:21], 0, v[188:189]
	v_lshl_add_u64 v[78:79], v[26:27], 0, v[14:15]
	global_load_dwordx4 v[30:33], v[24:25], off
	global_load_dwordx4 v[26:29], v[78:79], off
	s_waitcnt vmcnt(16)
	v_cvt_pk_bf16_f32 v6, v6, v7
	v_cvt_pk_bf16_f32 v7, v8, v9
	v_cvt_pk_bf16_f32 v8, v2, v3
	v_add_u32_e32 v2, 0, v208
	v_cvt_pk_bf16_f32 v9, v4, v5
	ds_write_b128 v2, v[6:9]
	s_waitcnt vmcnt(14)
	v_cvt_pk_bf16_f32 v2, v16, v17
	v_add_u32_e32 v6, 0, v205
	v_cvt_pk_bf16_f32 v3, v18, v19
	v_cvt_pk_bf16_f32 v4, v10, v11
	v_cvt_pk_bf16_f32 v5, v12, v13
	ds_write_b128 v6, v[2:5]
	v_add_u32_e32 v2, 0, v206
	s_waitcnt vmcnt(13)
	ds_write_b128 v2, v[20:23] offset:32768
	v_add_u32_e32 v2, 0, v207
	s_waitcnt vmcnt(12)
	ds_write_b128 v2, v[50:53] offset:32768
	s_waitcnt vmcnt(10)
	v_cvt_pk_bf16_f32 v2, v58, v59
	v_add_u32_e32 v6, 0, v204
	v_cvt_pk_bf16_f32 v3, v60, v61
	v_cvt_pk_bf16_f32 v4, v54, v55
	v_cvt_pk_bf16_f32 v5, v56, v57
	ds_write_b128 v6, v[2:5]
	s_waitcnt vmcnt(8)
	v_cvt_pk_bf16_f32 v2, v66, v67
	v_add_u32_e32 v6, 0, v201
	v_cvt_pk_bf16_f32 v3, v68, v69
	v_cvt_pk_bf16_f32 v4, v62, v63
	v_cvt_pk_bf16_f32 v5, v64, v65
	ds_write_b128 v6, v[2:5]
	v_add_u32_e32 v2, 0, v202
	s_waitcnt vmcnt(7)
	ds_write_b128 v2, v[70:73] offset:32768
	v_add_u32_e32 v2, 0, v203
	s_waitcnt vmcnt(6)
	ds_write_b128 v2, v[74:77] offset:32768
	v_lshl_add_u64 v[2:3], s[0:1], 0, v[190:191]
	v_lshl_add_u64 v[2:3], v[2:3], 0, v[182:183]
	global_load_dwordx4 v[6:9], v[2:3], off offset:16
	global_load_dwordx4 v[22:25], v[2:3], off
	v_lshl_add_u64 v[2:3], s[0:1], 0, v[192:193]
	v_lshl_add_u64 v[16:17], v[2:3], 0, v[182:183]
	global_load_dwordx4 v[2:5], v[16:17], off offset:16
	global_load_dwordx4 v[10:13], v[16:17], off
	v_lshl_add_u64 v[16:17], s[20:21], 0, v[194:195]
	v_lshl_add_u64 v[50:51], v[16:17], 0, v[14:15]
	v_lshl_add_u64 v[16:17], s[20:21], 0, v[196:197]
	v_lshl_add_u64 v[52:53], v[16:17], 0, v[14:15]
	global_load_dwordx4 v[18:21], v[50:51], off
	global_load_dwordx4 v[14:17], v[52:53], off
	v_lshlrev_b32_e32 v50, 13, v200
	s_cmp_lg_u32 0, -1
	s_cselect_b32 s0, 0, 0
	v_add3_u32 v209, v80, s0, v81
	s_add_i32 s0, s0, 0x8000
	v_add3_u32 v210, v50, s0, v81
	s_lshl_b32 s0, s30, 1
	s_add_i32 s31, s31, s0
	s_lshl_b32 s0, s2, 3
	s_add_i32 s0, s0, s31
	s_waitcnt lgkmcnt(0)
	s_and_b32 s0, s0, 15
	s_lshl_b32 s0, s0, 6
	s_add_i32 s22, s0, 0x80
	v_mov_b32_e32 v50, v183
	v_mov_b32_e32 v51, v183
	v_mov_b32_e32 v52, v183
	v_mov_b32_e32 v53, v183
	v_mov_b32_e32 v54, v183
	v_mov_b32_e32 v55, v183
	v_mov_b32_e32 v56, v183
	v_mov_b32_e32 v57, v183
	v_mov_b32_e32 v58, v183
	v_mov_b32_e32 v59, v183
	v_mov_b32_e32 v60, v183
	v_mov_b32_e32 v61, v183
	v_mov_b32_e32 v62, v183
	v_mov_b32_e32 v63, v183
	v_mov_b32_e32 v64, v183
	v_mov_b32_e32 v65, v183
	v_mov_b32_e32 v66, v183
	v_mov_b32_e32 v67, v183
	v_mov_b32_e32 v68, v183
	v_mov_b32_e32 v69, v183
	v_mov_b32_e32 v70, v183
	v_mov_b32_e32 v71, v183
	v_mov_b32_e32 v72, v183
	v_mov_b32_e32 v73, v183
	v_mov_b32_e32 v74, v183
	v_mov_b32_e32 v75, v183
	v_mov_b32_e32 v76, v183
	v_mov_b32_e32 v77, v183
	v_mov_b32_e32 v78, v183
	v_mov_b32_e32 v79, v183
	v_mov_b32_e32 v80, v183
	v_mov_b32_e32 v81, v183
	v_mov_b32_e32 v82, v183
	v_mov_b32_e32 v83, v183
	v_mov_b32_e32 v84, v183
	v_mov_b32_e32 v85, v183
	v_mov_b32_e32 v86, v183
	v_mov_b32_e32 v87, v183
	v_mov_b32_e32 v88, v183
	v_mov_b32_e32 v89, v183
	v_mov_b32_e32 v90, v183
	v_mov_b32_e32 v91, v183
	v_mov_b32_e32 v92, v183
	v_mov_b32_e32 v93, v183
	v_mov_b32_e32 v94, v183
	v_mov_b32_e32 v95, v183
	v_mov_b32_e32 v96, v183
	v_mov_b32_e32 v97, v183
	v_mov_b32_e32 v98, v183
	v_mov_b32_e32 v99, v183
	v_mov_b32_e32 v100, v183
	v_mov_b32_e32 v101, v183
	v_mov_b32_e32 v102, v183
	v_mov_b32_e32 v103, v183
	v_mov_b32_e32 v104, v183
	v_mov_b32_e32 v105, v183
	v_mov_b32_e32 v106, v183
	v_mov_b32_e32 v107, v183
	v_mov_b32_e32 v108, v183
	v_mov_b32_e32 v109, v183
	v_mov_b32_e32 v110, v183
	v_mov_b32_e32 v111, v183
	v_mov_b32_e32 v112, v183
	v_mov_b32_e32 v113, v183
	v_mov_b32_e32 v114, v183
	v_mov_b32_e32 v115, v183
	v_mov_b32_e32 v116, v183
	v_mov_b32_e32 v117, v183
	v_mov_b32_e32 v118, v183
	v_mov_b32_e32 v119, v183
	v_mov_b32_e32 v120, v183
	v_mov_b32_e32 v121, v183
	v_mov_b32_e32 v122, v183
	v_mov_b32_e32 v123, v183
	v_mov_b32_e32 v124, v183
	v_mov_b32_e32 v125, v183
	v_mov_b32_e32 v126, v183
	v_mov_b32_e32 v127, v183
	v_mov_b32_e32 v128, v183
	v_mov_b32_e32 v129, v183
	v_mov_b32_e32 v130, v183
	v_mov_b32_e32 v131, v183
	v_mov_b32_e32 v132, v183
	v_mov_b32_e32 v133, v183
	v_mov_b32_e32 v134, v183
	v_mov_b32_e32 v135, v183
	v_mov_b32_e32 v136, v183
	v_mov_b32_e32 v137, v183
	v_mov_b32_e32 v138, v183
	v_mov_b32_e32 v139, v183
	v_mov_b32_e32 v140, v183
	v_mov_b32_e32 v141, v183
	v_mov_b32_e32 v142, v183
	v_mov_b32_e32 v143, v183
	v_mov_b32_e32 v144, v183
	v_mov_b32_e32 v145, v183
	v_mov_b32_e32 v146, v183
	v_mov_b32_e32 v147, v183
	v_mov_b32_e32 v148, v183
	v_mov_b32_e32 v149, v183
	v_mov_b32_e32 v150, v183
	v_mov_b32_e32 v151, v183
	v_mov_b32_e32 v152, v183
	v_mov_b32_e32 v153, v183
	v_mov_b32_e32 v154, v183
	v_mov_b32_e32 v155, v183
	v_mov_b32_e32 v156, v183
	v_mov_b32_e32 v157, v183
	v_mov_b32_e32 v158, v183
	v_mov_b32_e32 v159, v183
	v_mov_b32_e32 v160, v183
	v_mov_b32_e32 v161, v183
	v_mov_b32_e32 v162, v183
	v_mov_b32_e32 v163, v183
	v_mov_b32_e32 v164, v183
	v_mov_b32_e32 v165, v183
	v_mov_b32_e32 v166, v183
	v_mov_b32_e32 v167, v183
	v_mov_b32_e32 v168, v183
	v_mov_b32_e32 v169, v183
	v_mov_b32_e32 v170, v183
	v_mov_b32_e32 v171, v183
	v_mov_b32_e32 v172, v183
	v_mov_b32_e32 v173, v183
	v_mov_b32_e32 v174, v183
	v_mov_b32_e32 v175, v183
	v_mov_b32_e32 v176, v183
	v_mov_b32_e32 v177, v183
	s_and_b32 s0, s29, 0x10000
	v_add_u32_e32 v211, s0, v209
	v_add_u32_e32 v242, s0, v210
	s_barrier
	.p2align	6
.LBB1_1:
	ds_read_b128 v[212:215], v242 offset:0
	ds_read_b128 v[216:219], v242 offset:0x800
	ds_read_b128 v[220:223], v242 offset:0x1000
	ds_read_b128 v[224:227], v242 offset:0x1800
	ds_read_b128 v[228:231], v211 offset:0
	ds_read_b128 v[232:235], v211 offset:0x800
	ds_read_b128 v[236:239], v211 offset:0x1000
	s_waitcnt lgkmcnt(2)
	v_mfma_f32_16x16x32_bf16 v[174:177], v[212:215], v[228:231], v[174:177]
	v_mfma_f32_16x16x32_bf16 v[170:173], v[216:219], v[228:231], v[170:173]
	v_mfma_f32_16x16x32_bf16 v[166:169], v[220:223], v[228:231], v[166:169]
	v_mfma_f32_16x16x32_bf16 v[162:165], v[224:227], v[228:231], v[162:165]
	ds_read_b128 v[228:231], v211 offset:0x1800
	s_waitcnt lgkmcnt(2)
	v_mfma_f32_16x16x32_bf16 v[158:161], v[212:215], v[232:235], v[158:161]
	v_mfma_f32_16x16x32_bf16 v[154:157], v[216:219], v[232:235], v[154:157]
	v_mfma_f32_16x16x32_bf16 v[150:153], v[220:223], v[232:235], v[150:153]
	v_mfma_f32_16x16x32_bf16 v[146:149], v[224:227], v[232:235], v[146:149]
	ds_read_b128 v[232:235], v211 offset:0x2000
	s_waitcnt lgkmcnt(2)
	v_mfma_f32_16x16x32_bf16 v[142:145], v[212:215], v[236:239], v[142:145]
	v_mfma_f32_16x16x32_bf16 v[138:141], v[216:219], v[236:239], v[138:141]
	v_mfma_f32_16x16x32_bf16 v[134:137], v[220:223], v[236:239], v[134:137]
	v_mfma_f32_16x16x32_bf16 v[130:133], v[224:227], v[236:239], v[130:133]
	ds_read_b128 v[236:239], v211 offset:0x2800
	s_waitcnt lgkmcnt(2)
	v_mfma_f32_16x16x32_bf16 v[126:129], v[212:215], v[228:231], v[126:129]
	v_mfma_f32_16x16x32_bf16 v[122:125], v[216:219], v[228:231], v[122:125]
	v_mfma_f32_16x16x32_bf16 v[118:121], v[220:223], v[228:231], v[118:121]
	v_mfma_f32_16x16x32_bf16 v[114:117], v[224:227], v[228:231], v[114:117]
	ds_read_b128 v[228:231], v211 offset:0x3000
	s_waitcnt lgkmcnt(2)
	v_mfma_f32_16x16x32_bf16 v[110:113], v[212:215], v[232:235], v[110:113]
	v_mfma_f32_16x16x32_bf16 v[106:109], v[216:219], v[232:235], v[106:109]
	v_mfma_f32_16x16x32_bf16 v[102:105], v[220:223], v[232:235], v[102:105]
	v_mfma_f32_16x16x32_bf16 v[98:101], v[224:227], v[232:235], v[98:101]
	ds_read_b128 v[232:235], v211 offset:0x3800
	s_waitcnt lgkmcnt(2)
	v_mfma_f32_16x16x32_bf16 v[94:97], v[212:215], v[236:239], v[94:97]
	v_mfma_f32_16x16x32_bf16 v[90:93], v[216:219], v[236:239], v[90:93]
	v_mfma_f32_16x16x32_bf16 v[86:89], v[220:223], v[236:239], v[86:89]
	v_mfma_f32_16x16x32_bf16 v[82:85], v[224:227], v[236:239], v[82:85]
	s_waitcnt lgkmcnt(1)
	v_mfma_f32_16x16x32_bf16 v[78:81], v[212:215], v[228:231], v[78:81]
	v_mfma_f32_16x16x32_bf16 v[74:77], v[216:219], v[228:231], v[74:77]
	v_mfma_f32_16x16x32_bf16 v[70:73], v[220:223], v[228:231], v[70:73]
	v_mfma_f32_16x16x32_bf16 v[66:69], v[224:227], v[228:231], v[66:69]
	s_waitcnt lgkmcnt(0)
	v_mfma_f32_16x16x32_bf16 v[62:65], v[212:215], v[232:235], v[62:65]
	v_mfma_f32_16x16x32_bf16 v[58:61], v[216:219], v[232:235], v[58:61]
	v_mfma_f32_16x16x32_bf16 v[54:57], v[220:223], v[232:235], v[54:57]
	v_mfma_f32_16x16x32_bf16 v[50:53], v[224:227], v[232:235], v[50:53]
	s_xor_b32 s0, s0, 0x10000
	s_and_b32 s1, s22, 0x3c0
	s_add_i32 s23, s0, 0
	s_lshl_b32 s0, s1, 2
	s_add_u32 s20, s25, s0
	s_waitcnt vmcnt(10)
	v_cvt_pk_bf16_f32 v46, v46, v47
	v_cvt_pk_bf16_f32 v47, v48, v49
	v_cvt_pk_bf16_f32 v48, v42, v43
	v_cvt_pk_bf16_f32 v49, v44, v45
	s_waitcnt vmcnt(8)
	v_cvt_pk_bf16_f32 v38, v38, v39
	v_cvt_pk_bf16_f32 v39, v40, v41
	v_cvt_pk_bf16_f32 v40, v34, v35
	v_add_u32_e32 v34, s23, v208
	s_addc_u32 s21, s26, 0
	s_lshl_b32 s0, s1, 1
	v_cvt_pk_bf16_f32 v41, v36, v37
	v_lshlrev_b32_e32 v182, 2, v178
	v_add_u32_e32 v35, s23, v205
	v_add_u32_e32 v36, s23, v206
	v_add_u32_e32 v37, s23, v207
	ds_write_b128 v34, v[46:49]
	ds_write_b128 v35, v[38:41]
	s_waitcnt vmcnt(7)
	ds_write_b128 v36, v[30:33] offset:32768
	s_waitcnt vmcnt(6)
	ds_write_b128 v37, v[26:29] offset:32768
	v_lshl_add_u64 v[26:27], s[20:21], 0, v[180:181]
	v_lshl_add_u64 v[28:29], s[20:21], 0, v[184:185]
	s_add_u32 s0, s27, s0
	v_lshl_add_u64 v[26:27], v[26:27], 0, v[182:183]
	v_lshl_add_u64 v[28:29], v[28:29], 0, v[182:183]
	s_addc_u32 s1, s28, 0
	v_lshlrev_b32_e32 v240, 1, v178
	v_mov_b32_e32 v241, v183
	global_load_dwordx4 v[42:45], v[26:27], off offset:16
	global_load_dwordx4 v[46:49], v[26:27], off
	global_load_dwordx4 v[34:37], v[28:29], off offset:16
	global_load_dwordx4 v[38:41], v[28:29], off
	v_lshl_add_u64 v[26:27], s[0:1], 0, v[186:187]
	v_lshl_add_u64 v[28:29], s[0:1], 0, v[188:189]
	v_lshl_add_u64 v[26:27], v[26:27], 0, v[240:241]
	v_lshl_add_u64 v[28:29], v[28:29], 0, v[240:241]
	global_load_dwordx4 v[30:33], v[26:27], off
	s_nop 0
	global_load_dwordx4 v[26:29], v[28:29], off
	ds_read_b128 v[212:215], v242 offset:0x400
	ds_read_b128 v[216:219], v242 offset:0xc00
	ds_read_b128 v[220:223], v242 offset:0x1400
	ds_read_b128 v[224:227], v242 offset:0x1c00
	ds_read_b128 v[228:231], v211 offset:0x400
	ds_read_b128 v[232:235], v211 offset:0xc00
	ds_read_b128 v[236:239], v211 offset:0x1400
	s_waitcnt lgkmcnt(2)
	v_mfma_f32_16x16x32_bf16 v[174:177], v[212:215], v[228:231], v[174:177]
	v_mfma_f32_16x16x32_bf16 v[170:173], v[216:219], v[228:231], v[170:173]
	v_mfma_f32_16x16x32_bf16 v[166:169], v[220:223], v[228:231], v[166:169]
	v_mfma_f32_16x16x32_bf16 v[162:165], v[224:227], v[228:231], v[162:165]
	ds_read_b128 v[228:231], v211 offset:0x1c00
	s_waitcnt lgkmcnt(2)
	v_mfma_f32_16x16x32_bf16 v[158:161], v[212:215], v[232:235], v[158:161]
	v_mfma_f32_16x16x32_bf16 v[154:157], v[216:219], v[232:235], v[154:157]
	v_mfma_f32_16x16x32_bf16 v[150:153], v[220:223], v[232:235], v[150:153]
	v_mfma_f32_16x16x32_bf16 v[146:149], v[224:227], v[232:235], v[146:149]
	ds_read_b128 v[232:235], v211 offset:0x2400
	s_waitcnt lgkmcnt(2)
	v_mfma_f32_16x16x32_bf16 v[142:145], v[212:215], v[236:239], v[142:145]
	v_mfma_f32_16x16x32_bf16 v[138:141], v[216:219], v[236:239], v[138:141]
	v_mfma_f32_16x16x32_bf16 v[134:137], v[220:223], v[236:239], v[134:137]
	v_mfma_f32_16x16x32_bf16 v[130:133], v[224:227], v[236:239], v[130:133]
	ds_read_b128 v[236:239], v211 offset:0x2c00
	s_waitcnt lgkmcnt(2)
	v_mfma_f32_16x16x32_bf16 v[126:129], v[212:215], v[228:231], v[126:129]
	v_mfma_f32_16x16x32_bf16 v[122:125], v[216:219], v[228:231], v[122:125]
	v_mfma_f32_16x16x32_bf16 v[118:121], v[220:223], v[228:231], v[118:121]
	v_mfma_f32_16x16x32_bf16 v[114:117], v[224:227], v[228:231], v[114:117]
	ds_read_b128 v[228:231], v211 offset:0x3400
	s_waitcnt lgkmcnt(2)
	v_mfma_f32_16x16x32_bf16 v[110:113], v[212:215], v[232:235], v[110:113]
	v_mfma_f32_16x16x32_bf16 v[106:109], v[216:219], v[232:235], v[106:109]
	v_mfma_f32_16x16x32_bf16 v[102:105], v[220:223], v[232:235], v[102:105]
	v_mfma_f32_16x16x32_bf16 v[98:101], v[224:227], v[232:235], v[98:101]
	ds_read_b128 v[232:235], v211 offset:0x3c00
	s_waitcnt lgkmcnt(2)
	v_mfma_f32_16x16x32_bf16 v[94:97], v[212:215], v[236:239], v[94:97]
	v_mfma_f32_16x16x32_bf16 v[90:93], v[216:219], v[236:239], v[90:93]
	v_mfma_f32_16x16x32_bf16 v[86:89], v[220:223], v[236:239], v[86:89]
	v_mfma_f32_16x16x32_bf16 v[82:85], v[224:227], v[236:239], v[82:85]
	s_waitcnt lgkmcnt(1)
	v_mfma_f32_16x16x32_bf16 v[78:81], v[212:215], v[228:231], v[78:81]
	v_mfma_f32_16x16x32_bf16 v[74:77], v[216:219], v[228:231], v[74:77]
	v_mfma_f32_16x16x32_bf16 v[70:73], v[220:223], v[228:231], v[70:73]
	v_mfma_f32_16x16x32_bf16 v[66:69], v[224:227], v[228:231], v[66:69]
	s_waitcnt lgkmcnt(0)
	v_mfma_f32_16x16x32_bf16 v[62:65], v[212:215], v[232:235], v[62:65]
	v_mfma_f32_16x16x32_bf16 v[58:61], v[216:219], v[232:235], v[58:61]
	v_mfma_f32_16x16x32_bf16 v[54:57], v[220:223], v[232:235], v[54:57]
	v_mfma_f32_16x16x32_bf16 v[50:53], v[224:227], v[232:235], v[50:53]
	s_waitcnt vmcnt(10)
	v_cvt_pk_bf16_f32 v22, v22, v23
	v_cvt_pk_bf16_f32 v23, v24, v25
	v_cvt_pk_bf16_f32 v24, v6, v7
	v_cvt_pk_bf16_f32 v25, v8, v9
	v_add_u32_e32 v6, s23, v204
	s_waitcnt vmcnt(9)
	v_cvt_pk_bf16_f32 v8, v2, v3
	v_add_u32_e32 v2, s23, v201
	ds_write_b128 v6, v[22:25]
	s_waitcnt vmcnt(8)
	v_cvt_pk_bf16_f32 v6, v10, v11
	v_cvt_pk_bf16_f32 v7, v12, v13
	v_cvt_pk_bf16_f32 v9, v4, v5
	ds_write_b128 v2, v[6:9]
	v_add_u32_e32 v2, s23, v202
	s_waitcnt vmcnt(7)
	ds_write_b128 v2, v[18:21] offset:32768
	v_add_u32_e32 v2, s23, v203
	s_waitcnt vmcnt(6)
	ds_write_b128 v2, v[14:17] offset:32768
	v_lshl_add_u64 v[2:3], s[20:21], 0, v[190:191]
	v_lshl_add_u64 v[2:3], v[2:3], 0, v[182:183]
	global_load_dwordx4 v[6:9], v[2:3], off offset:16
	global_load_dwordx4 v[22:25], v[2:3], off
	v_lshl_add_u64 v[2:3], s[20:21], 0, v[192:193]
	v_lshl_add_u64 v[14:15], s[0:1], 0, v[194:195]
	v_lshl_add_u64 v[16:17], s[0:1], 0, v[196:197]
	v_lshl_add_u64 v[10:11], v[2:3], 0, v[182:183]
	v_lshl_add_u64 v[14:15], v[14:15], 0, v[240:241]
	v_lshl_add_u64 v[16:17], v[16:17], 0, v[240:241]
	global_load_dwordx4 v[2:5], v[10:11], off offset:16
	s_nop 0
	global_load_dwordx4 v[10:13], v[10:11], off
	s_nop 0
	global_load_dwordx4 v[18:21], v[14:15], off
	s_nop 0
	global_load_dwordx4 v[14:17], v[16:17], off
	s_waitcnt lgkmcnt(0)
	s_add_i32 s22, s22, 64
	s_add_i32 s29, s29, 0x10000
	s_and_b32 s0, s29, 0x10000
	v_add_u32_e32 v211, s0, v209
	v_add_u32_e32 v242, s0, v210
	s_cmp_lg_u32 s29, 0xe0000
	s_barrier
	s_cbranch_scc1 .LBB1_1
	s_lshl_b64 s[0:1], s[18:19], 24
	ds_read_b128 v[180:183], v210 offset:0
	ds_read_b128 v[184:187], v210 offset:0x800
	ds_read_b128 v[188:191], v210 offset:0x1000
	ds_read_b128 v[192:195], v210 offset:0x1800
	ds_read_b128 v[212:215], v209 offset:0
	ds_read_b128 v[216:219], v209 offset:0x800
	ds_read_b128 v[220:223], v209 offset:0x1000
	s_waitcnt lgkmcnt(0)
	s_add_u32 s0, s10, s0
	s_addc_u32 s18, s11, s1
	s_lshl_b32 s19, s24, 1
	s_mov_b32 s1, 0
	s_add_u32 s0, s0, s19
	s_waitcnt lgkmcnt(2)
	s_addc_u32 s20, s18, 0
	v_mfma_f32_16x16x32_bf16 v[174:177], v[180:183], v[212:215], v[174:177]
	v_mfma_f32_16x16x32_bf16 v[170:173], v[184:187], v[212:215], v[170:173]
	v_mfma_f32_16x16x32_bf16 v[166:169], v[188:191], v[212:215], v[166:169]
	v_mfma_f32_16x16x32_bf16 v[162:165], v[192:195], v[212:215], v[162:165]
	ds_read_b128 v[212:215], v209 offset:0x1800
	s_waitcnt lgkmcnt(2)
	s_nop 0
	v_mfma_f32_16x16x32_bf16 v[158:161], v[180:183], v[216:219], v[158:161]
	v_mfma_f32_16x16x32_bf16 v[154:157], v[184:187], v[216:219], v[154:157]
	v_mfma_f32_16x16x32_bf16 v[150:153], v[188:191], v[216:219], v[150:153]
	v_mfma_f32_16x16x32_bf16 v[146:149], v[192:195], v[216:219], v[146:149]
	ds_read_b128 v[216:219], v209 offset:0x2000
	s_waitcnt lgkmcnt(2)
	s_nop 0
	v_mfma_f32_16x16x32_bf16 v[142:145], v[180:183], v[220:223], v[142:145]
	v_mfma_f32_16x16x32_bf16 v[138:141], v[184:187], v[220:223], v[138:141]
	v_mfma_f32_16x16x32_bf16 v[134:137], v[188:191], v[220:223], v[134:137]
	v_mfma_f32_16x16x32_bf16 v[130:133], v[192:195], v[220:223], v[130:133]
	ds_read_b128 v[220:223], v209 offset:0x2800
	s_waitcnt lgkmcnt(2)
	s_nop 0
	v_mfma_f32_16x16x32_bf16 v[126:129], v[180:183], v[212:215], v[126:129]
	v_mfma_f32_16x16x32_bf16 v[122:125], v[184:187], v[212:215], v[122:125]
	v_mfma_f32_16x16x32_bf16 v[118:121], v[188:191], v[212:215], v[118:121]
	v_mfma_f32_16x16x32_bf16 v[114:117], v[192:195], v[212:215], v[114:117]
	ds_read_b128 v[212:215], v209 offset:0x3000
	s_waitcnt lgkmcnt(2)
	s_nop 0
	v_mfma_f32_16x16x32_bf16 v[110:113], v[180:183], v[216:219], v[110:113]
	v_mfma_f32_16x16x32_bf16 v[106:109], v[184:187], v[216:219], v[106:109]
	v_mfma_f32_16x16x32_bf16 v[102:105], v[188:191], v[216:219], v[102:105]
	v_mfma_f32_16x16x32_bf16 v[98:101], v[192:195], v[216:219], v[98:101]
	ds_read_b128 v[216:219], v209 offset:0x3800
	s_waitcnt lgkmcnt(2)
	s_nop 0
	v_mfma_f32_16x16x32_bf16 v[94:97], v[180:183], v[220:223], v[94:97]
	v_mfma_f32_16x16x32_bf16 v[90:93], v[184:187], v[220:223], v[90:93]
	v_mfma_f32_16x16x32_bf16 v[86:89], v[188:191], v[220:223], v[86:89]
	v_mfma_f32_16x16x32_bf16 v[82:85], v[192:195], v[220:223], v[82:85]
	s_waitcnt lgkmcnt(1)
	s_nop 0
	v_mfma_f32_16x16x32_bf16 v[78:81], v[180:183], v[212:215], v[78:81]
	v_mfma_f32_16x16x32_bf16 v[74:77], v[184:187], v[212:215], v[74:77]
	v_mfma_f32_16x16x32_bf16 v[70:73], v[188:191], v[212:215], v[70:73]
	v_mfma_f32_16x16x32_bf16 v[66:69], v[192:195], v[212:215], v[66:69]
	s_waitcnt lgkmcnt(0)
	s_nop 0
	v_mfma_f32_16x16x32_bf16 v[62:65], v[180:183], v[216:219], v[62:65]
	v_mfma_f32_16x16x32_bf16 v[58:61], v[184:187], v[216:219], v[58:61]
	v_mfma_f32_16x16x32_bf16 v[54:57], v[188:191], v[216:219], v[54:57]
	v_mfma_f32_16x16x32_bf16 v[50:53], v[192:195], v[216:219], v[50:53]
	s_add_i32 s18, 0, 0x10000
	s_waitcnt vmcnt(10)
	v_cvt_pk_bf16_f32 v46, v46, v47
	v_cvt_pk_bf16_f32 v47, v48, v49
	v_cvt_pk_bf16_f32 v48, v42, v43
	v_add_u32_e32 v42, s18, v208
	s_waitcnt vmcnt(8)
	v_cvt_pk_bf16_f32 v38, v38, v39
	v_cvt_pk_bf16_f32 v39, v40, v41
	v_cvt_pk_bf16_f32 v40, v34, v35
	v_add_u32_e32 v34, s18, v205
	s_add_i32 s19, 0, 0x18000
	v_cvt_pk_bf16_f32 v49, v44, v45
	ds_write_b128 v42, v[46:49]
	v_cvt_pk_bf16_f32 v41, v36, v37
	ds_write_b128 v34, v[38:41]
	v_add_u32_e32 v34, s19, v206
	s_waitcnt vmcnt(7)
	ds_write_b128 v34, v[30:33]
	v_add_u32_e32 v30, s19, v207
	s_waitcnt vmcnt(6)
	ds_write_b128 v30, v[26:29]
	ds_read_b128 v[26:29], v210 offset:0x400
	ds_read_b128 v[30:33], v210 offset:0xc00
	ds_read_b128 v[34:37], v210 offset:0x1400
	ds_read_b128 v[38:41], v210 offset:0x1c00
	ds_read_b128 v[42:45], v209 offset:0x400
	ds_read_b128 v[46:49], v209 offset:0xc00
	ds_read_b128 v[180:183], v209 offset:0x1400
	s_nop 0
	s_waitcnt lgkmcnt(2)
	s_nop 0
	v_mfma_f32_16x16x32_bf16 v[174:177], v[26:29], v[42:45], v[174:177]
	v_mfma_f32_16x16x32_bf16 v[170:173], v[30:33], v[42:45], v[170:173]
	v_mfma_f32_16x16x32_bf16 v[166:169], v[34:37], v[42:45], v[166:169]
	v_mfma_f32_16x16x32_bf16 v[42:45], v[38:41], v[42:45], v[162:165]
	ds_read_b128 v[162:165], v209 offset:0x1c00
	s_waitcnt lgkmcnt(2)
	s_nop 0
	v_mfma_f32_16x16x32_bf16 v[158:161], v[26:29], v[46:49], v[158:161]
	v_mfma_f32_16x16x32_bf16 v[154:157], v[30:33], v[46:49], v[154:157]
	v_mfma_f32_16x16x32_bf16 v[150:153], v[34:37], v[46:49], v[150:153]
	v_mfma_f32_16x16x32_bf16 v[46:49], v[38:41], v[46:49], v[146:149]
	ds_read_b128 v[146:149], v209 offset:0x2400
	s_waitcnt lgkmcnt(2)
	s_nop 0
	v_mfma_f32_16x16x32_bf16 v[142:145], v[26:29], v[180:183], v[142:145]
	v_mfma_f32_16x16x32_bf16 v[138:141], v[30:33], v[180:183], v[138:141]
	v_mfma_f32_16x16x32_bf16 v[134:137], v[34:37], v[180:183], v[134:137]
	v_mfma_f32_16x16x32_bf16 v[130:133], v[38:41], v[180:183], v[130:133]
	ds_read_b128 v[180:183], v209 offset:0x2c00
	s_waitcnt lgkmcnt(2)
	s_nop 0
	v_mfma_f32_16x16x32_bf16 v[126:129], v[26:29], v[162:165], v[126:129]
	v_mfma_f32_16x16x32_bf16 v[122:125], v[30:33], v[162:165], v[122:125]
	v_mfma_f32_16x16x32_bf16 v[118:121], v[34:37], v[162:165], v[118:121]
	v_mfma_f32_16x16x32_bf16 v[114:117], v[38:41], v[162:165], v[114:117]
	ds_read_b128 v[162:165], v209 offset:0x3400
	s_waitcnt lgkmcnt(2)
	s_nop 0
	v_mfma_f32_16x16x32_bf16 v[110:113], v[26:29], v[146:149], v[110:113]
	v_mfma_f32_16x16x32_bf16 v[106:109], v[30:33], v[146:149], v[106:109]
	v_mfma_f32_16x16x32_bf16 v[102:105], v[34:37], v[146:149], v[102:105]
	v_mfma_f32_16x16x32_bf16 v[98:101], v[38:41], v[146:149], v[98:101]
	ds_read_b128 v[146:149], v209 offset:0x3c00
	s_waitcnt lgkmcnt(2)
	s_nop 0
	v_mfma_f32_16x16x32_bf16 v[94:97], v[26:29], v[180:183], v[94:97]
	v_mfma_f32_16x16x32_bf16 v[90:93], v[30:33], v[180:183], v[90:93]
	v_mfma_f32_16x16x32_bf16 v[86:89], v[34:37], v[180:183], v[86:89]
	v_mfma_f32_16x16x32_bf16 v[82:85], v[38:41], v[180:183], v[82:85]
	s_waitcnt lgkmcnt(1)
	s_nop 0
	v_mfma_f32_16x16x32_bf16 v[78:81], v[26:29], v[162:165], v[78:81]
	v_mfma_f32_16x16x32_bf16 v[74:77], v[30:33], v[162:165], v[74:77]
	v_mfma_f32_16x16x32_bf16 v[70:73], v[34:37], v[162:165], v[70:73]
	v_mfma_f32_16x16x32_bf16 v[66:69], v[38:41], v[162:165], v[66:69]
	s_waitcnt lgkmcnt(0)
	s_nop 0
	v_mfma_f32_16x16x32_bf16 v[26:29], v[26:29], v[146:149], v[62:65]
	v_mfma_f32_16x16x32_bf16 v[30:33], v[30:33], v[146:149], v[58:61]
	v_mfma_f32_16x16x32_bf16 v[34:37], v[34:37], v[146:149], v[54:57]
	v_mfma_f32_16x16x32_bf16 v[38:41], v[38:41], v[146:149], v[50:53]
	s_waitcnt vmcnt(4)
	v_cvt_pk_bf16_f32 v22, v22, v23
	v_cvt_pk_bf16_f32 v23, v24, v25
	v_cvt_pk_bf16_f32 v24, v6, v7
	v_cvt_pk_bf16_f32 v25, v8, v9
	v_add_u32_e32 v6, s18, v204
	s_waitcnt vmcnt(3)
	v_cvt_pk_bf16_f32 v8, v2, v3
	v_add_u32_e32 v2, s18, v201
	ds_write_b128 v6, v[22:25]
	s_waitcnt vmcnt(2)
	v_cvt_pk_bf16_f32 v6, v10, v11
	v_cvt_pk_bf16_f32 v7, v12, v13
	v_cvt_pk_bf16_f32 v9, v4, v5
	ds_write_b128 v2, v[6:9]
	v_add_u32_e32 v2, s19, v202
	s_waitcnt vmcnt(1)
	ds_write_b128 v2, v[18:21]
	v_add_u32_e32 v2, s19, v203
	s_waitcnt vmcnt(0)
	ds_write_b128 v2, v[14:17]
	s_waitcnt lgkmcnt(0)
	s_barrier
	v_add_u32_e32 v178, 0x10000, v209
	v_add_u32_e32 v196, 0x10000, v210
	ds_read_b128 v[2:5], v196 offset:0
	ds_read_b128 v[6:9], v196 offset:0x800
	ds_read_b128 v[10:13], v196 offset:0x1000
	ds_read_b128 v[14:17], v196 offset:0x1800
	ds_read_b128 v[18:21], v178 offset:0
	s_and_b64 s[16:17], s[16:17], exec
	ds_read_b128 v[22:25], v178 offset:0x800
	ds_read_b128 v[50:53], v178 offset:0x1000
	s_waitcnt lgkmcnt(2)
	s_cselect_b32 s5, s5, s7
	s_cselect_b32 s4, s4, s6
	s_lshl_b32 s6, s3, 10
	v_mfma_f32_16x16x32_bf16 v[54:57], v[2:5], v[18:21], v[174:177]
	s_add_u32 s6, s4, s6
	s_addc_u32 s7, s5, 0
	s_lshl_b32 s3, s3, 9
	v_mfma_f32_16x16x32_bf16 v[58:61], v[6:9], v[18:21], v[170:173]
	s_add_u32 s4, s0, s3
	s_addc_u32 s5, s20, 0
	v_mfma_f32_16x16x32_bf16 v[62:65], v[10:13], v[18:21], v[166:169]
	v_mfma_f32_16x16x32_bf16 v[18:21], v[14:17], v[18:21], v[42:45]
	ds_read_b128 v[42:45], v178 offset:0x1800
	s_waitcnt lgkmcnt(2)
	s_nop 0
	v_mfma_f32_16x16x32_bf16 v[146:149], v[2:5], v[22:25], v[158:161]
	v_mfma_f32_16x16x32_bf16 v[154:157], v[6:9], v[22:25], v[154:157]
	v_mfma_f32_16x16x32_bf16 v[150:153], v[10:13], v[22:25], v[150:153]
	v_mfma_f32_16x16x32_bf16 v[22:25], v[14:17], v[22:25], v[46:49]
	ds_read_b128 v[46:49], v178 offset:0x2000
	s_waitcnt lgkmcnt(2)
	s_nop 0
	v_mfma_f32_16x16x32_bf16 v[142:145], v[2:5], v[50:53], v[142:145]
	v_mfma_f32_16x16x32_bf16 v[138:141], v[6:9], v[50:53], v[138:141]
	v_mfma_f32_16x16x32_bf16 v[134:137], v[10:13], v[50:53], v[134:137]
	v_mfma_f32_16x16x32_bf16 v[50:53], v[14:17], v[50:53], v[130:133]
	ds_read_b128 v[130:133], v178 offset:0x2800
	s_waitcnt lgkmcnt(2)
	s_nop 0
	v_mfma_f32_16x16x32_bf16 v[126:129], v[2:5], v[42:45], v[126:129]
	v_mfma_f32_16x16x32_bf16 v[122:125], v[6:9], v[42:45], v[122:125]
	v_mfma_f32_16x16x32_bf16 v[118:121], v[10:13], v[42:45], v[118:121]
	v_mfma_f32_16x16x32_bf16 v[42:45], v[14:17], v[42:45], v[114:117]
	ds_read_b128 v[114:117], v178 offset:0x3000
	s_waitcnt lgkmcnt(2)
	s_nop 0
	v_mfma_f32_16x16x32_bf16 v[110:113], v[2:5], v[46:49], v[110:113]
	v_mfma_f32_16x16x32_bf16 v[106:109], v[6:9], v[46:49], v[106:109]
	v_mfma_f32_16x16x32_bf16 v[102:105], v[10:13], v[46:49], v[102:105]
	v_mfma_f32_16x16x32_bf16 v[98:101], v[14:17], v[46:49], v[98:101]
	ds_read_b128 v[46:49], v178 offset:0x3800
	s_waitcnt lgkmcnt(2)
	s_nop 0
	v_mfma_f32_16x16x32_bf16 v[158:161], v[2:5], v[130:133], v[94:97]
	v_mfma_f32_16x16x32_bf16 v[162:165], v[6:9], v[130:133], v[90:93]
	v_mfma_f32_16x16x32_bf16 v[166:169], v[10:13], v[130:133], v[86:89]
	v_mfma_f32_16x16x32_bf16 v[130:133], v[14:17], v[130:133], v[82:85]
	s_waitcnt lgkmcnt(1)
	s_nop 0
	v_mfma_f32_16x16x32_bf16 v[66:69], v[14:17], v[114:117], v[66:69]
	v_mfma_f32_16x16x32_bf16 v[170:173], v[2:5], v[114:117], v[78:81]
	v_mfma_f32_16x16x32_bf16 v[174:177], v[6:9], v[114:117], v[74:77]
	v_mfma_f32_16x16x32_bf16 v[180:183], v[10:13], v[114:117], v[70:73]
	s_waitcnt lgkmcnt(0)
	s_nop 0
	v_mfma_f32_16x16x32_bf16 v[2:5], v[2:5], v[46:49], v[26:29]
	v_mfma_f32_16x16x32_bf16 v[114:117], v[6:9], v[46:49], v[30:33]
	v_mfma_f32_16x16x32_bf16 v[34:37], v[10:13], v[46:49], v[34:37]
	v_mfma_f32_16x16x32_bf16 v[184:187], v[14:17], v[46:49], v[38:41]
	ds_read_b128 v[188:191], v196 offset:0x400
	ds_read_b128 v[192:195], v196 offset:0xc00
	ds_read_b128 v[202:205], v196 offset:0x1400
	ds_read_b128 v[206:209], v196 offset:0x1c00
	ds_read_b128 v[6:9], v178 offset:0x400
	ds_read_b128 v[10:13], v178 offset:0xc00
	ds_read_b128 v[14:17], v178 offset:0x1400
	s_nop 0
	s_waitcnt lgkmcnt(2)
	s_nop 0
	v_mfma_f32_16x16x32_bf16 v[94:97], v[192:195], v[6:9], v[58:61]
	v_mfma_f32_16x16x32_bf16 v[62:65], v[202:205], v[6:9], v[62:65]
	v_mfma_f32_16x16x32_bf16 v[30:33], v[206:209], v[6:9], v[18:21]
	v_mfma_f32_16x16x32_bf16 v[210:213], v[188:191], v[6:9], v[54:57]
	ds_read_b128 v[6:9], v178 offset:0x1c00
	s_waitcnt lgkmcnt(2)
	s_nop 0
	v_mfma_f32_16x16x32_bf16 v[90:93], v[192:195], v[10:13], v[154:157]
	v_mfma_f32_16x16x32_bf16 v[58:61], v[202:205], v[10:13], v[150:153]
	v_mfma_f32_16x16x32_bf16 v[26:29], v[206:209], v[10:13], v[22:25]
	v_mfma_f32_16x16x32_bf16 v[146:149], v[188:191], v[10:13], v[146:149]
	ds_read_b128 v[10:13], v178 offset:0x2400
	s_waitcnt lgkmcnt(2)
	s_nop 0
	v_mfma_f32_16x16x32_bf16 v[86:89], v[192:195], v[14:17], v[138:141]
	v_mfma_f32_16x16x32_bf16 v[54:57], v[202:205], v[14:17], v[134:137]
	v_mfma_f32_16x16x32_bf16 v[22:25], v[206:209], v[14:17], v[50:53]
	v_mfma_f32_16x16x32_bf16 v[142:145], v[188:191], v[14:17], v[142:145]
	ds_read_b128 v[38:41], v178 offset:0x2c00
	s_waitcnt lgkmcnt(2)
	s_nop 0
	v_mfma_f32_16x16x32_bf16 v[126:129], v[188:191], v[6:9], v[126:129]
	v_mfma_f32_16x16x32_bf16 v[82:85], v[192:195], v[6:9], v[122:125]
	v_mfma_f32_16x16x32_bf16 v[50:53], v[202:205], v[6:9], v[118:121]
	v_mfma_f32_16x16x32_bf16 v[18:21], v[206:209], v[6:9], v[42:45]
	ds_read_b128 v[6:9], v178 offset:0x3400
	s_waitcnt lgkmcnt(2)
	s_nop 0
	v_mfma_f32_16x16x32_bf16 v[110:113], v[188:191], v[10:13], v[110:113]
	v_mfma_f32_16x16x32_bf16 v[78:81], v[192:195], v[10:13], v[106:109]
	v_mfma_f32_16x16x32_bf16 v[46:49], v[202:205], v[10:13], v[102:105]
	v_mfma_f32_16x16x32_bf16 v[14:17], v[206:209], v[10:13], v[98:101]
	ds_read_b128 v[98:101], v178 offset:0x3c00
	s_waitcnt lgkmcnt(2)
	s_nop 0
	v_mfma_f32_16x16x32_bf16 v[106:109], v[188:191], v[38:41], v[158:161]
	v_mfma_f32_16x16x32_bf16 v[74:77], v[192:195], v[38:41], v[162:165]
	v_mfma_f32_16x16x32_bf16 v[42:45], v[202:205], v[38:41], v[166:169]
	v_mfma_f32_16x16x32_bf16 v[10:13], v[206:209], v[38:41], v[130:133]
	s_waitcnt lgkmcnt(1)
	s_nop 0
	v_mfma_f32_16x16x32_bf16 v[118:121], v[188:191], v[6:9], v[170:173]
	v_mfma_f32_16x16x32_bf16 v[70:73], v[192:195], v[6:9], v[174:177]
	v_mfma_f32_16x16x32_bf16 v[38:41], v[202:205], v[6:9], v[180:183]
	v_mfma_f32_16x16x32_bf16 v[6:9], v[206:209], v[6:9], v[66:69]
	s_waitcnt lgkmcnt(0)
	s_nop 0
	v_mfma_f32_16x16x32_bf16 v[122:125], v[188:191], v[98:101], v[2:5]
	v_mfma_f32_16x16x32_bf16 v[66:69], v[192:195], v[98:101], v[114:117]
	v_mfma_f32_16x16x32_bf16 v[34:37], v[202:205], v[98:101], v[34:37]
	v_mfma_f32_16x16x32_bf16 v[2:5], v[206:209], v[98:101], v[184:187]
	v_lshrrev_b32_e32 v98, 2, v199
	v_and_b32_e32 v98, 12, v98
	v_lshl_or_b32 v104, v200, 6, v98
	v_lshlrev_b32_e32 v105, 2, v104
	s_waitcnt lgkmcnt(0)
	s_barrier
	global_load_dwordx4 v[114:117], v105, s[6:7]
	v_lshrrev_b32_e32 v98, 1, v199
	v_lshlrev_b32_e32 v99, 16, v198
	v_lshlrev_b32_e32 v100, 9, v179
	v_and_b32_e32 v102, 8, v98
	v_lshrrev_b32_e32 v98, 3, v104
	v_add3_u32 v103, 0, v99, v100
	v_xor_b32_e32 v130, v98, v179
	v_bitop3_b32 v131, v98, v179, 16 bitop3:0x1e
	global_load_dwordx4 v[98:101], v105, s[6:7] offset:64
	v_lshlrev_b32_e32 v130, 4, v130
	v_lshlrev_b32_e32 v131, 4, v131
	v_add3_u32 v130, v103, v130, v102
	v_add3_u32 v131, v103, v131, v102
	s_movk_i32 s0, 0x200
	s_waitcnt vmcnt(1)
	v_add_f32_e32 v132, v210, v114
	v_add_f32_e32 v133, v211, v115
	v_add_f32_e32 v134, v212, v116
	v_add_f32_e32 v135, v213, v117
	v_add_f32_e32 v140, v142, v114
	v_add_f32_e32 v141, v143, v115
	v_add_f32_e32 v142, v144, v116
	v_add_f32_e32 v143, v145, v117
	v_add_f32_e32 v110, v110, v114
	v_add_f32_e32 v111, v111, v115
	v_add_f32_e32 v106, v106, v114
	v_add_f32_e32 v107, v107, v115
	v_add_f32_e32 v136, v146, v114
	v_add_f32_e32 v137, v147, v115
	v_add_f32_e32 v138, v148, v116
	v_add_f32_e32 v139, v149, v117
	v_add_f32_e32 v126, v126, v114
	v_add_f32_e32 v127, v127, v115
	v_add_f32_e32 v128, v128, v116
	v_add_f32_e32 v129, v129, v117
	v_add_f32_e32 v112, v112, v116
	v_add_f32_e32 v113, v113, v117
	v_add_f32_e32 v108, v108, v116
	v_add_f32_e32 v109, v109, v117
	v_max_f32_e32 v132, 0, v132
	v_max_f32_e32 v133, 0, v133
	v_max_f32_e32 v134, 0, v134
	v_max_f32_e32 v135, 0, v135
	v_max_f32_e32 v140, 0, v140
	v_max_f32_e32 v141, 0, v141
	v_max_f32_e32 v142, 0, v142
	v_max_f32_e32 v143, 0, v143
	v_max_f32_e32 v144, 0, v110
	v_max_f32_e32 v145, 0, v111
	v_max_f32_e32 v148, 0, v106
	v_max_f32_e32 v149, 0, v107
	v_cvt_pk_bf16_f32 v106, v132, v133
	v_cvt_pk_bf16_f32 v107, v134, v135
	v_cvt_pk_bf16_f32 v110, v140, v141
	v_cvt_pk_bf16_f32 v111, v142, v143
	v_add_f32_e32 v118, v118, v114
	v_add_f32_e32 v119, v119, v115
	v_max_f32_e32 v136, 0, v136
	v_max_f32_e32 v137, 0, v137
	v_max_f32_e32 v138, 0, v138
	v_max_f32_e32 v139, 0, v139
	v_max_f32_e32 v126, 0, v126
	v_max_f32_e32 v127, 0, v127
	v_max_f32_e32 v128, 0, v128
	v_max_f32_e32 v129, 0, v129
	v_max_f32_e32 v146, 0, v112
	v_max_f32_e32 v147, 0, v113
	v_max_f32_e32 v150, 0, v108
	v_max_f32_e32 v151, 0, v109
	v_cvt_pk_bf16_f32 v108, v136, v137
	v_cvt_pk_bf16_f32 v109, v138, v139
	v_cvt_pk_bf16_f32 v112, v126, v127
	v_cvt_pk_bf16_f32 v113, v128, v129
	ds_write2st64_b64 v130, v[106:107], v[110:111] offset1:32
	ds_write2st64_b64 v131, v[108:109], v[112:113] offset0:16 offset1:48
	v_add_f32_e32 v106, v121, v117
	v_add_f32_e32 v120, v120, v116
	v_max_f32_e32 v152, 0, v118
	v_max_f32_e32 v153, 0, v119
	v_max_f32_e32 v107, 0, v106
	v_cvt_pk_bf16_f32 v106, v152, v153
	v_max_f32_e32 v120, 0, v120
	v_cvt_pk_bf16_f32 v118, v144, v145
	v_cvt_pk_bf16_f32 v119, v146, v147
	v_cvt_pk_bf16_f32 v107, v120, v107
	ds_write2st64_b64 v130, v[118:119], v[106:107] offset0:64 offset1:96
	v_add_f32_e32 v106, v122, v114
	v_max_f32_e32 v106, 0, v106
	v_add_f32_e32 v107, v123, v115
	v_max_f32_e32 v107, 0, v107
	v_add_f32_e32 v108, v124, v116
	v_add_f32_e32 v109, v125, v117
	v_cvt_pk_bf16_f32 v106, v106, v107
	v_cvt_pk_bf16_f32 v126, v148, v149
	v_cvt_pk_bf16_f32 v127, v150, v151
	v_max_f32_e32 v108, 0, v108
	v_max_f32_e32 v109, 0, v109
	v_cvt_pk_bf16_f32 v107, v108, v109
	ds_write2st64_b64 v131, v[126:127], v[106:107] offset0:80 offset1:112
	v_or_b32_e32 v106, 16, v104
	s_waitcnt vmcnt(0)
	v_add_f32_e32 v94, v94, v98
	v_add_f32_e32 v95, v95, v99
	v_add_f32_e32 v96, v96, v100
	v_lshrrev_b32_e32 v106, 3, v106
	v_max_f32_e32 v94, 0, v94
	v_max_f32_e32 v95, 0, v95
	v_max_f32_e32 v96, 0, v96
	v_add_f32_e32 v97, v97, v101
	v_max_f32_e32 v97, 0, v97
	v_cvt_pk_bf16_f32 v94, v94, v95
	v_cvt_pk_bf16_f32 v95, v96, v97
	v_xor_b32_e32 v96, v106, v179
	v_lshlrev_b32_e32 v96, 4, v96
	v_add3_u32 v107, v103, v96, v102
	v_add_f32_e32 v90, v90, v98
	v_add_f32_e32 v91, v91, v99
	v_add_f32_e32 v92, v92, v100
	ds_write_b64 v107, v[94:95]
	v_max_f32_e32 v90, 0, v90
	v_max_f32_e32 v91, 0, v91
	global_load_dwordx4 v[94:97], v105, s[6:7] offset:128
	v_max_f32_e32 v92, 0, v92
	v_add_f32_e32 v93, v93, v101
	v_max_f32_e32 v93, 0, v93
	v_cvt_pk_bf16_f32 v90, v90, v91
	v_cvt_pk_bf16_f32 v91, v92, v93
	v_bitop3_b32 v92, v106, v179, 16 bitop3:0x1e
	v_add_f32_e32 v66, v66, v98
	v_lshlrev_b32_e32 v92, 4, v92
	v_add_f32_e32 v86, v86, v98
	v_add_f32_e32 v87, v87, v99
	v_add_f32_e32 v82, v82, v98
	v_add_f32_e32 v83, v83, v99
	v_add_f32_e32 v78, v78, v98
	v_add_f32_e32 v79, v79, v99
	v_add_f32_e32 v74, v74, v98
	v_add_f32_e32 v75, v75, v99
	v_add_f32_e32 v70, v70, v98
	v_add_f32_e32 v71, v71, v99
	v_max_f32_e32 v66, 0, v66
	v_add_f32_e32 v67, v67, v99
	v_add3_u32 v92, v103, v92, v102
	v_max_f32_e32 v86, 0, v86
	v_max_f32_e32 v87, 0, v87
	v_add_f32_e32 v88, v88, v100
	v_add_f32_e32 v89, v89, v101
	v_max_f32_e32 v82, 0, v82
	v_max_f32_e32 v83, 0, v83
	v_add_f32_e32 v84, v84, v100
	v_add_f32_e32 v85, v85, v101
	v_max_f32_e32 v78, 0, v78
	v_max_f32_e32 v79, 0, v79
	v_add_f32_e32 v80, v80, v100
	v_add_f32_e32 v81, v81, v101
	v_max_f32_e32 v74, 0, v74
	v_max_f32_e32 v75, 0, v75
	v_add_f32_e32 v76, v76, v100
	v_add_f32_e32 v77, v77, v101
	v_max_f32_e32 v70, 0, v70
	v_max_f32_e32 v71, 0, v71
	v_add_f32_e32 v72, v72, v100
	v_add_f32_e32 v73, v73, v101
	v_max_f32_e32 v67, 0, v67
	v_add_f32_e32 v68, v68, v100
	v_add_f32_e32 v69, v69, v101
	v_cvt_pk_bf16_f32 v66, v66, v67
	ds_write_b64 v92, v[90:91] offset:8192
	v_max_f32_e32 v88, 0, v88
	v_max_f32_e32 v89, 0, v89
	v_cvt_pk_bf16_f32 v86, v86, v87
	v_cvt_pk_bf16_f32 v87, v88, v89
	ds_write_b64 v107, v[86:87] offset:16384
	v_max_f32_e32 v84, 0, v84
	v_max_f32_e32 v85, 0, v85
	v_cvt_pk_bf16_f32 v82, v82, v83
	v_cvt_pk_bf16_f32 v83, v84, v85
	ds_write_b64 v92, v[82:83] offset:24576
	v_max_f32_e32 v80, 0, v80
	v_max_f32_e32 v81, 0, v81
	v_cvt_pk_bf16_f32 v78, v78, v79
	v_cvt_pk_bf16_f32 v79, v80, v81
	ds_write_b64 v107, v[78:79] offset:32768
	v_max_f32_e32 v76, 0, v76
	v_max_f32_e32 v77, 0, v77
	v_cvt_pk_bf16_f32 v74, v74, v75
	v_cvt_pk_bf16_f32 v75, v76, v77
	ds_write_b64 v92, v[74:75] offset:40960
	v_max_f32_e32 v72, 0, v72
	v_max_f32_e32 v73, 0, v73
	v_cvt_pk_bf16_f32 v70, v70, v71
	v_cvt_pk_bf16_f32 v71, v72, v73
	ds_write_b64 v107, v[70:71] offset:49152
	v_max_f32_e32 v68, 0, v68
	v_max_f32_e32 v69, 0, v69
	v_cvt_pk_bf16_f32 v67, v68, v69
	ds_write_b64 v92, v[66:67] offset:57344
	v_or_b32_e32 v66, 32, v104
	v_lshrrev_b32_e32 v70, 3, v66
	global_load_dwordx4 v[66:69], v105, s[6:7] offset:192
	s_waitcnt vmcnt(1)
	v_add_f32_e32 v62, v62, v94
	v_add_f32_e32 v63, v63, v95
	v_add_f32_e32 v64, v64, v96
	v_add_f32_e32 v58, v58, v94
	v_add_f32_e32 v59, v59, v95
	v_add_f32_e32 v60, v60, v96
	v_max_f32_e32 v62, 0, v62
	v_max_f32_e32 v63, 0, v63
	v_max_f32_e32 v64, 0, v64
	v_add_f32_e32 v65, v65, v97
	v_max_f32_e32 v58, 0, v58
	v_max_f32_e32 v59, 0, v59
	v_max_f32_e32 v60, 0, v60
	v_add_f32_e32 v61, v61, v97
	v_max_f32_e32 v65, 0, v65
	v_cvt_pk_bf16_f32 v62, v62, v63
	v_cvt_pk_bf16_f32 v63, v64, v65
	v_xor_b32_e32 v64, v70, v179
	v_max_f32_e32 v61, 0, v61
	v_cvt_pk_bf16_f32 v58, v58, v59
	v_cvt_pk_bf16_f32 v59, v60, v61
	v_bitop3_b32 v60, v70, v179, 16 bitop3:0x1e
	v_add_f32_e32 v34, v34, v94
	v_lshlrev_b32_e32 v64, 4, v64
	v_lshlrev_b32_e32 v60, 4, v60
	v_add_f32_e32 v54, v54, v94
	v_add_f32_e32 v55, v55, v95
	v_add_f32_e32 v50, v50, v94
	v_add_f32_e32 v51, v51, v95
	v_add_f32_e32 v46, v46, v94
	v_add_f32_e32 v47, v47, v95
	v_add_f32_e32 v42, v42, v94
	v_add_f32_e32 v43, v43, v95
	v_add_f32_e32 v38, v38, v94
	v_add_f32_e32 v39, v39, v95
	v_max_f32_e32 v34, 0, v34
	v_add_f32_e32 v35, v35, v95
	v_add3_u32 v64, v103, v64, v102
	v_add3_u32 v60, v103, v60, v102
	v_max_f32_e32 v54, 0, v54
	v_max_f32_e32 v55, 0, v55
	v_add_f32_e32 v56, v56, v96
	v_add_f32_e32 v57, v57, v97
	v_max_f32_e32 v50, 0, v50
	v_max_f32_e32 v51, 0, v51
	v_add_f32_e32 v52, v52, v96
	v_add_f32_e32 v53, v53, v97
	v_max_f32_e32 v46, 0, v46
	v_max_f32_e32 v47, 0, v47
	v_add_f32_e32 v48, v48, v96
	v_add_f32_e32 v49, v49, v97
	v_max_f32_e32 v42, 0, v42
	v_max_f32_e32 v43, 0, v43
	v_add_f32_e32 v44, v44, v96
	v_add_f32_e32 v45, v45, v97
	v_max_f32_e32 v38, 0, v38
	v_max_f32_e32 v39, 0, v39
	v_add_f32_e32 v40, v40, v96
	v_add_f32_e32 v41, v41, v97
	v_max_f32_e32 v35, 0, v35
	v_add_f32_e32 v36, v36, v96
	v_add_f32_e32 v37, v37, v97
	v_cvt_pk_bf16_f32 v34, v34, v35
	ds_write_b64 v64, v[62:63]
	ds_write_b64 v60, v[58:59] offset:8192
	v_max_f32_e32 v56, 0, v56
	v_max_f32_e32 v57, 0, v57
	v_cvt_pk_bf16_f32 v54, v54, v55
	v_cvt_pk_bf16_f32 v55, v56, v57
	ds_write_b64 v64, v[54:55] offset:16384
	v_max_f32_e32 v52, 0, v52
	v_max_f32_e32 v53, 0, v53
	v_cvt_pk_bf16_f32 v50, v50, v51
	v_cvt_pk_bf16_f32 v51, v52, v53
	ds_write_b64 v60, v[50:51] offset:24576
	v_max_f32_e32 v48, 0, v48
	v_max_f32_e32 v49, 0, v49
	v_cvt_pk_bf16_f32 v46, v46, v47
	v_cvt_pk_bf16_f32 v47, v48, v49
	ds_write_b64 v64, v[46:47] offset:32768
	v_max_f32_e32 v44, 0, v44
	v_max_f32_e32 v45, 0, v45
	v_cvt_pk_bf16_f32 v42, v42, v43
	v_cvt_pk_bf16_f32 v43, v44, v45
	ds_write_b64 v60, v[42:43] offset:40960
	v_max_f32_e32 v40, 0, v40
	v_max_f32_e32 v41, 0, v41
	v_cvt_pk_bf16_f32 v38, v38, v39
	v_cvt_pk_bf16_f32 v39, v40, v41
	ds_write_b64 v64, v[38:39] offset:49152
	v_max_f32_e32 v36, 0, v36
	v_max_f32_e32 v37, 0, v37
	v_cvt_pk_bf16_f32 v35, v36, v37
	ds_write_b64 v60, v[34:35] offset:57344
	v_or_b32_e32 v34, 48, v104
	s_waitcnt vmcnt(0)
	v_add_f32_e32 v30, v30, v66
	v_add_f32_e32 v31, v31, v67
	v_add_f32_e32 v32, v32, v68
	v_add_f32_e32 v26, v26, v66
	v_add_f32_e32 v27, v27, v67
	v_add_f32_e32 v28, v28, v68
	v_lshrrev_b32_e32 v34, 3, v34
	v_max_f32_e32 v30, 0, v30
	v_max_f32_e32 v31, 0, v31
	v_max_f32_e32 v32, 0, v32
	v_add_f32_e32 v33, v33, v69
	v_max_f32_e32 v26, 0, v26
	v_max_f32_e32 v27, 0, v27
	v_max_f32_e32 v28, 0, v28
	v_add_f32_e32 v29, v29, v69
	v_max_f32_e32 v33, 0, v33
	v_cvt_pk_bf16_f32 v30, v30, v31
	v_cvt_pk_bf16_f32 v31, v32, v33
	v_xor_b32_e32 v32, v34, v179
	v_max_f32_e32 v29, 0, v29
	v_cvt_pk_bf16_f32 v26, v26, v27
	v_cvt_pk_bf16_f32 v27, v28, v29
	v_bitop3_b32 v28, v34, v179, 16 bitop3:0x1e
	v_add_f32_e32 v2, v2, v66
	v_lshlrev_b32_e32 v32, 4, v32
	v_lshlrev_b32_e32 v28, 4, v28
	v_add_f32_e32 v22, v22, v66
	v_add_f32_e32 v23, v23, v67
	v_add_f32_e32 v18, v18, v66
	v_add_f32_e32 v19, v19, v67
	v_add_f32_e32 v14, v14, v66
	v_add_f32_e32 v15, v15, v67
	v_add_f32_e32 v10, v10, v66
	v_add_f32_e32 v11, v11, v67
	v_add_f32_e32 v6, v6, v66
	v_add_f32_e32 v7, v7, v67
	v_max_f32_e32 v2, 0, v2
	v_add_f32_e32 v3, v3, v67
	v_add3_u32 v32, v103, v32, v102
	v_add3_u32 v28, v103, v28, v102
	v_max_f32_e32 v22, 0, v22
	v_max_f32_e32 v23, 0, v23
	v_add_f32_e32 v24, v24, v68
	v_add_f32_e32 v25, v25, v69
	v_max_f32_e32 v18, 0, v18
	v_max_f32_e32 v19, 0, v19
	v_add_f32_e32 v20, v20, v68
	v_add_f32_e32 v21, v21, v69
	v_max_f32_e32 v14, 0, v14
	v_max_f32_e32 v15, 0, v15
	v_add_f32_e32 v16, v16, v68
	v_add_f32_e32 v17, v17, v69
	v_max_f32_e32 v10, 0, v10
	v_max_f32_e32 v11, 0, v11
	v_add_f32_e32 v12, v12, v68
	v_add_f32_e32 v13, v13, v69
	v_max_f32_e32 v6, 0, v6
	v_max_f32_e32 v7, 0, v7
	v_add_f32_e32 v8, v8, v68
	v_add_f32_e32 v9, v9, v69
	v_max_f32_e32 v3, 0, v3
	v_add_f32_e32 v4, v4, v68
	v_add_f32_e32 v5, v5, v69
	v_cvt_pk_bf16_f32 v2, v2, v3
	ds_write_b64 v32, v[30:31]
	ds_write_b64 v28, v[26:27] offset:8192
	v_max_f32_e32 v24, 0, v24
	v_max_f32_e32 v25, 0, v25
	v_cvt_pk_bf16_f32 v22, v22, v23
	v_cvt_pk_bf16_f32 v23, v24, v25
	ds_write_b64 v32, v[22:23] offset:16384
	v_max_f32_e32 v20, 0, v20
	v_max_f32_e32 v21, 0, v21
	v_cvt_pk_bf16_f32 v18, v18, v19
	v_cvt_pk_bf16_f32 v19, v20, v21
	ds_write_b64 v28, v[18:19] offset:24576
	v_max_f32_e32 v16, 0, v16
	v_max_f32_e32 v17, 0, v17
	v_cvt_pk_bf16_f32 v14, v14, v15
	v_cvt_pk_bf16_f32 v15, v16, v17
	ds_write_b64 v32, v[14:15] offset:32768
	v_max_f32_e32 v12, 0, v12
	v_max_f32_e32 v13, 0, v13
	v_cvt_pk_bf16_f32 v10, v10, v11
	v_cvt_pk_bf16_f32 v11, v12, v13
	ds_write_b64 v28, v[10:11] offset:40960
	v_max_f32_e32 v8, 0, v8
	v_max_f32_e32 v9, 0, v9
	v_cvt_pk_bf16_f32 v6, v6, v7
	v_cvt_pk_bf16_f32 v7, v8, v9
	ds_write_b64 v32, v[6:7] offset:49152
	v_max_f32_e32 v4, 0, v4
	v_max_f32_e32 v5, 0, v5
	v_cvt_pk_bf16_f32 v3, v4, v5
	ds_write_b64 v28, v[2:3] offset:57344
	v_and_b32_e32 v2, 0x1f0, v1
	v_lshrrev_b32_e32 v1, 5, v0
	v_xor_b32_e32 v4, v1, v0
	v_mov_b32_e32 v3, 0
	v_lshlrev_b32_e32 v4, 4, v4
	v_lshl_add_u64 v[12:13], s[4:5], 0, v[2:3]
	v_lshlrev_b32_e32 v2, 9, v1
	v_and_b32_e32 v16, 0x1f0, v4
	v_add3_u32 v2, 0, v2, v16
	s_waitcnt lgkmcnt(0)
	s_barrier
	ds_read_b128 v[4:7], v2
	v_lshlrev_b32_e32 v2, 11, v1
	v_lshl_add_u64 v[14:15], v[12:13], 0, v[2:3]
	v_or_b32_e32 v2, 0x200, v0
	v_lshrrev_b32_e32 v2, 5, v2
	v_xor_b32_e32 v9, v2, v0
	v_lshlrev_b32_e32 v9, 4, v9
	v_lshlrev_b32_e32 v8, 9, v2
	v_and_b32_e32 v9, 0x1f0, v9
	v_add3_u32 v8, 0, v8, v9
	ds_read_b128 v[8:11], v8
	v_lshlrev_b32_e32 v2, 11, v2
	s_waitcnt lgkmcnt(1)
	global_store_dwordx4 v[14:15], v[4:7], off sc1
	s_nop 1
	v_lshl_add_u64 v[4:5], v[12:13], 0, v[2:3]
	s_waitcnt lgkmcnt(0)
	global_store_dwordx4 v[4:5], v[8:11], off sc1
	v_or_b32_e32 v2, 32, v1
	v_lshlrev_b32_e32 v4, 9, v2
	v_or_b32_e32 v8, 0x600, v0
	v_lshrrev_b32_e32 v17, 5, v8
	v_xor_b32_e32 v9, v17, v0
	v_lshlrev_b32_e32 v9, 4, v9
	v_add3_u32 v4, 0, v4, v16
	v_lshlrev_b32_e32 v8, 9, v17
	v_and_b32_e32 v9, 0x1f0, v9
	ds_read_b128 v[4:7], v4
	v_add3_u32 v8, 0, v8, v9
	ds_read_b128 v[8:11], v8
	v_lshlrev_b32_e32 v2, 11, v2
	v_lshl_add_u64 v[14:15], v[12:13], 0, v[2:3]
	v_lshlrev_b32_e32 v2, 11, v17
	s_waitcnt lgkmcnt(1)
	global_store_dwordx4 v[14:15], v[4:7], off sc1
	s_nop 1
	v_lshl_add_u64 v[4:5], v[12:13], 0, v[2:3]
	s_waitcnt lgkmcnt(0)
	global_store_dwordx4 v[4:5], v[8:11], off sc1
	v_or_b32_e32 v2, 64, v1
	v_lshlrev_b32_e32 v4, 9, v2
	v_or_b32_e32 v8, 0xa00, v0
	v_lshrrev_b32_e32 v17, 5, v8
	v_xor_b32_e32 v9, v17, v0
	v_lshlrev_b32_e32 v9, 4, v9
	v_add3_u32 v4, 0, v4, v16
	v_lshlrev_b32_e32 v8, 9, v17
	v_and_b32_e32 v9, 0x1f0, v9
	ds_read_b128 v[4:7], v4
	v_add3_u32 v8, 0, v8, v9
	ds_read_b128 v[8:11], v8
	v_lshlrev_b32_e32 v2, 11, v2
	v_lshl_add_u64 v[14:15], v[12:13], 0, v[2:3]
	v_lshlrev_b32_e32 v2, 11, v17
	s_waitcnt lgkmcnt(1)
	global_store_dwordx4 v[14:15], v[4:7], off sc1
	s_nop 1
	v_lshl_add_u64 v[4:5], v[12:13], 0, v[2:3]
	s_waitcnt lgkmcnt(0)
	global_store_dwordx4 v[4:5], v[8:11], off sc1
	v_or_b32_e32 v2, 0x60, v1
	v_lshlrev_b32_e32 v4, 9, v2
	v_or_b32_e32 v8, 0xe00, v0
	v_lshrrev_b32_e32 v17, 5, v8
	v_xor_b32_e32 v9, v17, v0
	v_lshlrev_b32_e32 v9, 4, v9
	v_add3_u32 v4, 0, v4, v16
	v_lshlrev_b32_e32 v8, 9, v17
	v_and_b32_e32 v9, 0x1f0, v9
	ds_read_b128 v[4:7], v4
	v_add3_u32 v8, 0, v8, v9
	ds_read_b128 v[8:11], v8
	v_lshlrev_b32_e32 v2, 11, v2
	v_lshl_add_u64 v[14:15], v[12:13], 0, v[2:3]
	v_lshlrev_b32_e32 v2, 11, v17
	s_waitcnt lgkmcnt(1)
	global_store_dwordx4 v[14:15], v[4:7], off sc1
	s_nop 1
	v_lshl_add_u64 v[4:5], v[12:13], 0, v[2:3]
	s_waitcnt lgkmcnt(0)
	global_store_dwordx4 v[4:5], v[8:11], off sc1
	v_or_b32_e32 v2, 0x80, v1
	v_lshlrev_b32_e32 v4, 9, v2
	v_or_b32_e32 v8, 0x1200, v0
	v_lshrrev_b32_e32 v17, 5, v8
	v_xor_b32_e32 v9, v17, v0
	v_lshlrev_b32_e32 v9, 4, v9
	v_add3_u32 v4, 0, v4, v16
	v_lshlrev_b32_e32 v8, 9, v17
	v_and_b32_e32 v9, 0x1f0, v9
	ds_read_b128 v[4:7], v4
	v_add3_u32 v8, 0, v8, v9
	ds_read_b128 v[8:11], v8
	v_lshlrev_b32_e32 v2, 11, v2
	v_lshl_add_u64 v[14:15], v[12:13], 0, v[2:3]
	v_lshlrev_b32_e32 v2, 11, v17
	s_waitcnt lgkmcnt(1)
	global_store_dwordx4 v[14:15], v[4:7], off sc1
	s_nop 1
	v_lshl_add_u64 v[4:5], v[12:13], 0, v[2:3]
	s_waitcnt lgkmcnt(0)
	global_store_dwordx4 v[4:5], v[8:11], off sc1
	v_or_b32_e32 v2, 0xa0, v1
	v_lshlrev_b32_e32 v4, 9, v2
	v_or_b32_e32 v8, 0x1600, v0
	v_lshrrev_b32_e32 v17, 5, v8
	v_xor_b32_e32 v9, v17, v0
	v_lshlrev_b32_e32 v9, 4, v9
	v_add3_u32 v4, 0, v4, v16
	v_lshlrev_b32_e32 v8, 9, v17
	v_and_b32_e32 v9, 0x1f0, v9
	ds_read_b128 v[4:7], v4
	v_add3_u32 v8, 0, v8, v9
	ds_read_b128 v[8:11], v8
	v_lshlrev_b32_e32 v2, 11, v2
	v_lshl_add_u64 v[14:15], v[12:13], 0, v[2:3]
	v_lshlrev_b32_e32 v2, 11, v17
	s_waitcnt lgkmcnt(1)
	global_store_dwordx4 v[14:15], v[4:7], off sc1
	s_nop 1
	v_lshl_add_u64 v[4:5], v[12:13], 0, v[2:3]
	s_waitcnt lgkmcnt(0)
	global_store_dwordx4 v[4:5], v[8:11], off sc1
	v_or_b32_e32 v2, 0xc0, v1
	v_lshlrev_b32_e32 v4, 9, v2
	v_or_b32_e32 v8, 0x1a00, v0
	v_lshrrev_b32_e32 v17, 5, v8
	v_xor_b32_e32 v9, v17, v0
	v_add3_u32 v4, 0, v4, v16
	v_lshlrev_b32_e32 v9, 4, v9
	ds_read_b128 v[4:7], v4
	v_lshlrev_b32_e32 v8, 9, v17
	v_and_b32_e32 v9, 0x1f0, v9
	v_add3_u32 v8, 0, v8, v9
	ds_read_b128 v[8:11], v8
	v_lshlrev_b32_e32 v2, 11, v2
	v_lshl_add_u64 v[14:15], v[12:13], 0, v[2:3]
	v_lshlrev_b32_e32 v2, 11, v17
	v_or_b32_e32 v1, 0xe0, v1
	s_waitcnt lgkmcnt(1)
	global_store_dwordx4 v[14:15], v[4:7], off sc1
	s_nop 1
	v_lshl_add_u64 v[4:5], v[12:13], 0, v[2:3]
	v_lshlrev_b32_e32 v2, 9, v1
	v_add3_u32 v2, 0, v2, v16
	s_waitcnt lgkmcnt(0)
	global_store_dwordx4 v[4:5], v[8:11], off sc1
	ds_read_b128 v[4:7], v2
	v_lshlrev_b32_e32 v2, 11, v1
	v_or_b32_e32 v1, 0x1e00, v0
	v_lshrrev_b32_e32 v1, 5, v1
	v_xor_b32_e32 v9, v1, v0
	v_lshlrev_b32_e32 v9, 4, v9
	v_lshlrev_b32_e32 v8, 9, v1
	v_and_b32_e32 v9, 0x1f0, v9
	v_add3_u32 v8, 0, v8, v9
	ds_read_b128 v[8:11], v8
	v_lshl_add_u64 v[14:15], v[12:13], 0, v[2:3]
	v_lshlrev_b32_e32 v2, 11, v1
	s_waitcnt lgkmcnt(1)
	global_store_dwordx4 v[14:15], v[4:7], off sc1
	s_nop 1
	v_lshl_add_u64 v[4:5], v[12:13], 0, v[2:3]
	s_waitcnt lgkmcnt(0)
	global_store_dwordx4 v[4:5], v[8:11], off sc1
	s_waitcnt lgkmcnt(0)
	s_barrier
	s_lshl_b32 s3, s2, 3
	s_and_b32 s3, s3, 56
	s_ashr_i32 s17, s2, 5
	s_add_i32 s20, s3, s17
	s_ashr_i32 s21, s20, 31
	s_bfe_u32 s16, s2, 0x20003
	s_lshl_b64 s[4:5], s[20:21], 17
	s_lshl_b64 s[6:7], s[20:21], 19
	s_add_u32 s6, s12, s6
	s_addc_u32 s7, s13, s7
	s_lshl_b32 s3, s16, 19
	s_add_u32 s3, s14, s3
	v_ashrrev_i32_e32 v2, 6, v0
	v_lshlrev_b32_e32 v1, 4, v0
	s_addc_u32 s13, s15, 0
	v_lshlrev_b32_e32 v4, 9, v2
	v_and_b32_e32 v5, 0x1f0, v1
	s_add_u32 s12, s3, 0x400000
	v_and_or_b32 v32, v4, s0, v5
	v_lshlrev_b32_e32 v4, 5, v2
	v_and_b32_e32 v5, 48, v1
	s_addc_u32 s13, s13, 0
	v_bitop3_b32 v4, v4, v5, 32 bitop3:0x6c
	s_and_b32 s15, s2, 8
	s_add_i32 s3, s20, 3
	v_bfe_u32 v31, v0, 5, 1
	v_lshrrev_b32_e32 v34, 1, v4
	v_add_u32_e32 v4, s15, v2
	s_mov_b32 s20, 0x3ffffe
	v_and_or_b32 v30, v4, s20, v31
	v_bfe_i32 v5, v30, 0, 22
	v_bfe_u32 v4, v30, 21, 1
	v_add_u32_e32 v6, v5, v4
	v_lshlrev_b32_e32 v4, 3, v6
	v_and_b32_e32 v6, 0x7fffffe, v6
	s_lshl_b32 s0, s17, 4
	v_sub_u32_e32 v5, v5, v6
	s_and_b32 s17, s0, 16
	v_lshl_or_b32 v6, v5, 5, v34
	v_add_u32_e32 v5, s17, v2
	v_and_or_b32 v35, v5, s20, v31
	v_bfe_i32 v7, v35, 0, 22
	v_bfe_u32 v8, v35, 21, 1
	v_add_u32_e32 v8, v7, v8
	v_lshlrev_b32_e32 v9, 3, v8
	v_and_b32_e32 v8, 0x7fffffe, v8
	v_add_u32_e32 v5, 8, v5
	v_sub_u32_e32 v7, v7, v8
	v_and_or_b32 v36, v5, s20, v31
	v_lshl_or_b32 v98, v7, 5, v34
	v_bfe_i32 v5, v36, 0, 22
	v_bfe_u32 v7, v36, 21, 1
	v_add_u32_e32 v7, v5, v7
	v_lshrrev_b32_e32 v33, 6, v32
	v_lshlrev_b32_e32 v8, 3, v7
	v_and_b32_e32 v7, 0x7fffffe, v7
	s_and_b32 s3, s3, 15
	v_and_or_b32 v4, v4, -16, v33
	v_sub_u32_e32 v5, v5, v7
	v_and_or_b32 v14, v9, -16, v33
	v_lshl_or_b32 v100, v5, 5, v34
	v_ashrrev_i32_e32 v5, 31, v4
	s_lshl_b32 s14, s3, 6
	s_lshl_b32 s0, s3, 8
	s_lshl_b32 s2, s3, 7
	v_and_or_b32 v16, v8, -16, v33
	v_lshlrev_b64 v[4:5], 12, v[4:5]
	s_add_u32 s2, s12, s2
	v_ashrrev_i32_e32 v15, 31, v14
	v_lshl_add_u64 v[4:5], s[6:7], 0, v[4:5]
	v_ashrrev_i32_e32 v7, 31, v6
	s_addc_u32 s3, s13, 0
	v_lshlrev_b64 v[102:103], 11, v[14:15]
	v_ashrrev_i32_e32 v99, 31, v98
	v_ashrrev_i32_e32 v17, 31, v16
	v_lshl_add_u64 v[8:9], v[4:5], 0, s[0:1]
	v_lshlrev_b64 v[38:39], 2, v[6:7]
	v_lshl_add_u64 v[14:15], s[2:3], 0, v[102:103]
	v_lshlrev_b64 v[22:23], 1, v[98:99]
	v_lshlrev_b64 v[104:105], 11, v[16:17]
	v_ashrrev_i32_e32 v101, 31, v100
	v_lshl_add_u64 v[18:19], v[8:9], 0, v[38:39]
	v_lshl_add_u64 v[24:25], v[14:15], 0, v[22:23]
	v_lshl_add_u64 v[14:15], s[2:3], 0, v[104:105]
	v_lshlrev_b64 v[26:27], 1, v[100:101]
	global_load_dwordx4 v[6:9], v[18:19], off offset:16
	global_load_dwordx4 v[10:13], v[18:19], off
	v_lshl_add_u64 v[28:29], v[14:15], 0, v[26:27]
	global_load_dwordx4 v[14:17], v[24:25], off
	global_load_dwordx4 v[18:21], v[28:29], off
	v_lshlrev_b32_e32 v24, 10, v30
	v_or_b32_e32 v125, v24, v32
	v_xad_u32 v24, s15, 8, v2
	v_and_or_b32 v24, v24, s20, v31
	v_lshlrev_b32_e32 v25, 10, v24
	v_or_b32_e32 v122, v25, v32
	v_bfe_i32 v25, v24, 0, 22
	v_bfe_u32 v24, v24, 21, 1
	v_add_u32_e32 v28, v25, v24
	v_lshlrev_b32_e32 v24, 3, v28
	v_and_b32_e32 v28, 0x7fffffe, v28
	v_sub_u32_e32 v25, v25, v28
	v_lshl_or_b32 v28, v25, 5, v34
	v_lshlrev_b32_e32 v25, 10, v35
	v_or_b32_e32 v126, v25, v32
	v_lshlrev_b32_e32 v25, 10, v36
	v_or_b32_e32 v127, v25, v32
	v_xad_u32 v25, s17, 16, v2
	v_and_or_b32 v25, v25, s20, v31
	v_lshlrev_b32_e32 v29, 10, v25
	v_or_b32_e32 v123, v29, v32
	v_bfe_i32 v29, v25, 0, 22
	v_bfe_u32 v25, v25, 21, 1
	v_add_u32_e32 v25, v29, v25
	v_and_b32_e32 v121, 3, v2
	v_lshlrev_b32_e32 v30, 3, v25
	v_and_b32_e32 v25, 0x7fffffe, v25
	v_xad_u32 v2, s17, 24, v2
	v_sub_u32_e32 v25, v29, v25
	v_and_or_b32 v2, v2, s20, v31
	v_lshl_or_b32 v106, v25, 5, v34
	v_lshlrev_b32_e32 v25, 10, v2
	v_or_b32_e32 v124, v25, v32
	v_bfe_i32 v25, v2, 0, 22
	v_bfe_u32 v2, v2, 21, 1
	v_add_u32_e32 v2, v25, v2
	v_lshlrev_b32_e32 v29, 3, v2
	v_and_b32_e32 v2, 0x7fffffe, v2
	v_and_b32_e32 v118, 15, v0
	v_sub_u32_e32 v2, v25, v2
	v_lshlrev_b32_e32 v25, 2, v0
	v_ashrrev_i32_e32 v120, 8, v0
	v_and_or_b32 v32, v29, -16, v33
	v_lshl_or_b32 v108, v2, 5, v34
	v_and_b32_e32 v2, 48, v0
	v_and_b32_e32 v25, 32, v25
	v_lshlrev_b32_e32 v29, 6, v118
	v_and_b32_e32 v119, 63, v0
	v_and_or_b32 v24, v24, -16, v33
	v_and_or_b32 v30, v30, -16, v33
	v_lshlrev_b32_e32 v68, 13, v120
	v_bitop3_b32 v2, v29, v25, v2 bitop3:0x36
	v_ashrrev_i32_e32 v25, 31, v24
	v_lshlrev_b64 v[24:25], 12, v[24:25]
	v_lshl_add_u64 v[56:57], s[6:7], 0, v[24:25]
	v_ashrrev_i32_e32 v29, 31, v28
	v_lshl_add_u64 v[24:25], v[56:57], 0, s[0:1]
	v_lshlrev_b64 v[58:59], 2, v[28:29]
	v_ashrrev_i32_e32 v31, 31, v30
	v_lshl_add_u64 v[24:25], v[24:25], 0, v[58:59]
	v_lshlrev_b64 v[110:111], 11, v[30:31]
	v_ashrrev_i32_e32 v107, 31, v106
	v_ashrrev_i32_e32 v33, 31, v32
	global_load_dwordx4 v[40:43], v[24:25], off offset:16
	global_load_dwordx4 v[44:47], v[24:25], off
	v_lshl_add_u64 v[24:25], s[2:3], 0, v[110:111]
	v_lshlrev_b64 v[60:61], 1, v[106:107]
	v_lshlrev_b64 v[112:113], 11, v[32:33]
	v_ashrrev_i32_e32 v109, 31, v108
	v_lshl_add_u64 v[24:25], v[24:25], 0, v[60:61]
	v_lshl_add_u64 v[28:29], s[2:3], 0, v[112:113]
	v_lshlrev_b64 v[62:63], 1, v[108:109]
	v_lshl_add_u64 v[28:29], v[28:29], 0, v[62:63]
	global_load_dwordx4 v[48:51], v[24:25], off
	global_load_dwordx4 v[52:55], v[28:29], off
	s_add_i32 s0, s14, 64
	s_and_b32 s2, s0, 0x3c0
	s_lshl_b32 s0, s2, 2
	s_lshl_b32 s2, s2, 1
	v_lshl_add_u64 v[24:25], v[4:5], 0, s[0:1]
	s_add_u32 s2, s12, s2
	v_lshl_add_u64 v[24:25], v[24:25], 0, v[38:39]
	s_addc_u32 s3, s13, 0
	global_load_dwordx4 v[30:33], v[24:25], off offset:16
	global_load_dwordx4 v[34:37], v[24:25], off
	v_lshl_add_u64 v[24:25], s[2:3], 0, v[102:103]
	v_lshl_add_u64 v[64:65], v[24:25], 0, v[22:23]
	v_lshl_add_u64 v[22:23], s[2:3], 0, v[104:105]
	v_lshl_add_u64 v[66:67], v[22:23], 0, v[26:27]
	global_load_dwordx4 v[26:29], v[64:65], off
	global_load_dwordx4 v[22:25], v[66:67], off
	v_add_u32_e32 v64, 0, v125
	s_waitcnt vmcnt(10)
	v_cvt_pk_bf16_f32 v10, v10, v11
	v_cvt_pk_bf16_f32 v11, v12, v13
	v_cvt_pk_bf16_f32 v12, v6, v7
	v_add_u32_e32 v6, 0, v126
	v_cvt_pk_bf16_f32 v13, v8, v9
	ds_write_b128 v64, v[10:13]
	s_waitcnt vmcnt(9)
	ds_write_b128 v6, v[14:17] offset:32768
	v_add_u32_e32 v6, 0, v127
	s_waitcnt vmcnt(8)
	ds_write_b128 v6, v[18:21] offset:32768
	v_add_u32_e32 v10, 0, v122
	s_waitcnt vmcnt(6)
	v_cvt_pk_bf16_f32 v6, v44, v45
	v_cvt_pk_bf16_f32 v7, v46, v47
	v_cvt_pk_bf16_f32 v8, v40, v41
	v_cvt_pk_bf16_f32 v9, v42, v43
	ds_write_b128 v10, v[6:9]
	v_add_u32_e32 v6, 0, v123
	s_waitcnt vmcnt(5)
	ds_write_b128 v6, v[48:51] offset:32768
	v_add_u32_e32 v6, 0, v124
	s_waitcnt vmcnt(4)
	ds_write_b128 v6, v[52:55] offset:32768
	v_lshl_add_u64 v[6:7], v[56:57], 0, s[0:1]
	v_lshl_add_u64 v[14:15], v[6:7], 0, v[58:59]
	global_load_dwordx4 v[6:9], v[14:15], off offset:16
	global_load_dwordx4 v[10:13], v[14:15], off
	v_lshl_add_u64 v[14:15], s[2:3], 0, v[110:111]
	v_lshl_add_u64 v[40:41], v[14:15], 0, v[60:61]
	v_lshl_add_u64 v[14:15], s[2:3], 0, v[112:113]
	v_lshl_add_u64 v[42:43], v[14:15], 0, v[62:63]
	global_load_dwordx4 v[18:21], v[40:41], off
	global_load_dwordx4 v[14:17], v[42:43], off
	v_lshlrev_b32_e32 v40, 13, v121
	s_cmp_lg_u32 0, -1
	s_waitcnt lgkmcnt(0)
	s_cselect_b32 s0, 0, 0
	v_add3_u32 v128, v68, s0, v2
	s_add_i32 s0, s0, 0x8000
	v_add3_u32 v129, v40, s0, v2
	v_lshl_add_u64 v[114:115], v[4:5], 0, v[38:39]
	v_lshl_add_u64 v[116:117], v[56:57], 0, v[58:59]
	s_add_i32 s2, s14, 0x80
	s_mov_b32 s3, 0
	v_mov_b32_e32 v2, v3
	v_mov_b32_e32 v4, v3
	v_mov_b32_e32 v5, v3
	v_mov_b32_e32 v38, v3
	v_mov_b32_e32 v39, v3
	v_mov_b32_e32 v40, v3
	v_mov_b32_e32 v41, v3
	v_mov_b32_e32 v42, v3
	v_mov_b32_e32 v43, v3
	v_mov_b32_e32 v44, v3
	v_mov_b32_e32 v45, v3
	v_mov_b32_e32 v46, v3
	v_mov_b32_e32 v47, v3
	v_mov_b32_e32 v48, v3
	v_mov_b32_e32 v49, v3
	v_mov_b32_e32 v50, v3
	v_mov_b32_e32 v51, v3
	v_mov_b32_e32 v52, v3
	v_mov_b32_e32 v53, v3
	v_mov_b32_e32 v54, v3
	v_mov_b32_e32 v55, v3
	v_mov_b32_e32 v56, v3
	v_mov_b32_e32 v57, v3
	v_mov_b32_e32 v58, v3
	v_mov_b32_e32 v59, v3
	v_mov_b32_e32 v60, v3
	v_mov_b32_e32 v61, v3
	v_mov_b32_e32 v62, v3
	v_mov_b32_e32 v63, v3
	v_mov_b32_e32 v64, v3
	v_mov_b32_e32 v65, v3
	v_mov_b32_e32 v66, v3
	v_mov_b32_e32 v67, v3
	v_mov_b32_e32 v68, v3
	v_mov_b32_e32 v69, v3
	v_mov_b32_e32 v70, v3
	v_mov_b32_e32 v71, v3
	v_mov_b32_e32 v72, v3
	v_mov_b32_e32 v73, v3
	v_mov_b32_e32 v74, v3
	v_mov_b32_e32 v75, v3
	v_mov_b32_e32 v76, v3
	v_mov_b32_e32 v77, v3
	v_mov_b32_e32 v78, v3
	v_mov_b32_e32 v79, v3
	v_mov_b32_e32 v80, v3
	v_mov_b32_e32 v81, v3
	v_mov_b32_e32 v82, v3
	v_mov_b32_e32 v83, v3
	v_mov_b32_e32 v84, v3
	v_mov_b32_e32 v85, v3
	v_mov_b32_e32 v86, v3
	v_mov_b32_e32 v87, v3
	v_mov_b32_e32 v88, v3
	v_mov_b32_e32 v89, v3
	v_mov_b32_e32 v90, v3
	v_mov_b32_e32 v91, v3
	v_mov_b32_e32 v92, v3
	v_mov_b32_e32 v93, v3
	v_mov_b32_e32 v94, v3
	v_mov_b32_e32 v95, v3
	v_mov_b32_e32 v96, v3
	v_mov_b32_e32 v97, v3
	s_and_b32 s0, s3, 0x10000
	v_add_u32_e32 v158, s0, v128
	v_add_u32_e32 v159, s0, v129
	s_barrier
	.p2align	6
